# HGRN intra-block output via fragment-major scratch (2 coalesced dwordx4 loads in the recurrence instead of 8 dword loads); QT written from the LDS tile with one dwordx4 per thread
# speedup vs baseline: 1.0315x; 1.0052x over previous
; #define LAS __attribute__((address_space(3)))
; __device__ __forceinline__ void hgrn_x1_unit(const Args& a, int layer, int unit, LAS unsigned char* lds) {
;     int tid = threadIdx.x; asm volatile("" : "+v"(tid)); const int lane = tid & 63; const int wave = __builtin_amdgcn_readfirstlane(tid >> 6);
;     size_t wz_ = 0; asm volatile("" : "+s"(wz_)); unsigned char* ws = a.ws + wz_;
;     const int blk = unit & 63, h = (unit >> 6) & 7, b = unit >> 9;
;     const bf16* PROJ = (const bf16*)(ws + WS_PROJ);
;     bf16* QT = (bf16*)(ws + WS_HQT); bf16* KT = (bf16*)(ws + WS_HKT) + (size_t)unit * 4096; bf16* VT = (bf16*)(ws + WS_HVT) + (size_t)unit * 4096;
;     float* DEC = (float*)(ws + WS_HDEC) + (size_t)unit * 128; float* OI = (float*)(ws + WS_HOI);
;     LAS float* TOT = (LAS float*)(lds + HX_TOT);
;     const size_t tok0 = (size_t)b * SEQ + blk * HB;
;     const int d = tid & 127, tq = tid >> 7;
;     const float lb = ((const float*)(ws + WS_LB))[layer * 1024 + h * 128 + d];
;     float q[8], kk[8], c[8]; unsigned short vv[8];
;     float run = 0.f;
; #pragma unroll
;     for (int i = 0; i < 8; ++i) {
;         const bf16* pr = PROJ + (tok0 + 8 * tq + i) * DIN + h * 128 + d;
;         q[i] = bf2f(pr[C_QA]); vv[i] = pr[C_IA];
;         float z = bf2f(pr[C_FA]); z = fminf(fmaxf(z, -30.f), 30.f);
;         const float e = __expf(-z), sp = 1.0f / (1.0f + e), sn = e / (1.0f + e);
;         const float f = lb + (1.0f - lb) * sp; kk[i] = (1.0f - lb) * sn;
;         run += __logf(f); c[i] = run;
; template <int LAYER>
; __device__ __forceinline__ void layer_phases(const Args& args, LAS unsigned char* lds, const XcdBarrier& bar, int lo, int hi) {
;     ...
;         for (;;) {
;             __syncthreads();
;             if (threadIdx.x == 0) *slot = (int)__hip_atomic_fetch_add(ctr, 1u, __ATOMIC_RELAXED, __HIP_MEMORY_SCOPE_AGENT);
;             __syncthreads();
;             const int it = __builtin_amdgcn_readfirstlane(*slot);
;             if (it >= 256 + 1024 + 2048) break;
;             if (it < 256) s5_unit(args, LAYER, it, lds);
;             else if (it < 1280) { const int j = it - 256, n = 31 - (j >> 5), b = (j >> 3) & 3, hp = j & 7, n0_ = (b & 1) ? 31 - n : n; attn_item(args, LAYER, b * 256 + n0_ * 8 + hp, lds); }
;             else hgrn_x1_unit(args, LAYER, it - 1280, lds);
.LBB0_321:
	s_or_b64 exec, exec, s[4:5]
	s_waitcnt lgkmcnt(0)
	s_barrier
	ds_read_b32 v2, v1
	s_mov_b64 s[4:5], -1
	s_waitcnt lgkmcnt(0)
	v_readfirstlane_b32 s85, v2
	s_cmpk_gt_i32 s85, 0xcff
	s_cbranch_scc1 .LBB0_316
	s_cmpk_gt_i32 s85, 0xff
	s_cbranch_scc0 .LBB0_349
	s_cmpk_gt_u32 s85, 0x4ff
	s_cbranch_scc0 .LBB0_327
	s_add_i32 s22, s85, 0xfffffb00
	v_mov_b32_e32 v14, v0
	s_mov_b64 s[4:5], 0
	s_add_u32 s8, s20, s4
	s_addc_u32 s9, s21, s5
	s_lshl_b32 s4, s22, 2
	s_lshl_b32 s5, s22, 5
	s_and_b32 s4, s4, 0x1800
	s_and_b32 s5, s5, 0x7e0
	s_or_b32 s10, s4, s5
	s_lshl_b32 s4, s22, 1
	v_and_b32_e32 v15, 0x7f, v14
	s_and_b32 s12, s4, 0x380
	v_or_b32_e32 v2, s12, v15
	v_lshlrev_b32_e32 v82, 2, v2
	v_lshl_add_u64 v[2:3], s[8:9], 0, v[82:83]
	s_mov_b32 s4, 0x21480000
	v_add_co_u32_e32 v10, vcc, s4, v2
	s_lshl_b32 s4, s12, 1
	v_ashrrev_i32_e32 v16, 7, v14
	s_add_u32 s4, s8, s4
	v_lshlrev_b32_e32 v2, 3, v16
	v_lshlrev_b32_e32 v82, 1, v15
	s_addc_u32 s5, s9, 0
	s_mov_b32 s11, s23
	v_addc_co_u32_e32 v11, vcc, 0, v3, vcc
	v_ashrrev_i32_e32 v3, 31, v2
	v_lshl_add_u64 v[6:7], s[4:5], 0, v[82:83]
	s_mov_b64 s[4:5], 0x2d482000
	v_lshl_add_u64 v[4:5], v[2:3], 0, s[10:11]
	v_lshl_add_u64 v[8:9], v[6:7], 0, s[4:5]
	v_mad_i64_i32 v[8:9], s[4:5], v4, s72, v[8:9]
	s_movk_i32 s5, 0x6000
	s_nop 0
	v_add_co_u32_e32 v12, vcc, s5, v8
	s_movk_i32 s4, 0x5000
	s_nop 0
	v_addc_co_u32_e32 v13, vcc, 0, v9, vcc
	global_load_dword v23, v[10:11], off
	global_load_ushort v20, v[12:13], off
	global_load_ushort v21, v[8:9], off offset:2048
	v_add_co_u32_e32 v10, vcc, s4, v8
	s_movk_i32 s4, 0x1000
	s_nop 0
	v_addc_co_u32_e32 v11, vcc, 0, v9, vcc
	s_waitcnt vmcnt(18)
	v_add_co_u32_e32 v18, vcc, s4, v8
	s_mov_b32 s4, 0xb000
	s_nop 0
	v_addc_co_u32_e32 v19, vcc, 0, v9, vcc
	global_load_ushort v17, v[12:13], off offset:2048
	s_nop 0
	global_load_ushort v18, v[18:19], off
	s_nop 0
	global_load_ushort v12, v[8:9], off
	global_load_ushort v13, v[10:11], off offset:2048
	v_add_co_u32_e32 v10, vcc, s4, v8
	v_lshlrev_b64 v[4:5], 11, v[4:5]
	s_nop 0
	v_addc_co_u32_e32 v11, vcc, 0, v9, vcc
	global_load_ushort v36, v[10:11], off offset:2048
	v_readfirstlane_b32 s13, v14
	s_waitcnt vmcnt(7)
	v_sub_f32_e32 v24, 1.0, v23
	s_waitcnt vmcnt(6)
	v_lshlrev_b32_e32 v11, 16, v20
	s_waitcnt vmcnt(5)
	v_lshlrev_b32_e32 v10, 16, v21
	v_max_f32_e32 v10, v10, v10
	v_med3_f32 v10, v10, s73, v102
	v_mul_f32_e32 v10, 0xbfb8aa3b, v10
	v_exp_f32_e32 v10, v10
	v_max_f32_e32 v11, v11, v11
	v_med3_f32 v11, v11, s73, v102
	v_mul_f32_e32 v11, 0xbfb8aa3b, v11
	v_exp_f32_e32 v37, v11
	v_add_f32_e32 v11, 1.0, v10
	s_waitcnt vmcnt(2)
	v_lshlrev_b32_e32 v20, 16, v12
	v_div_scale_f32 v12, s[4:5], v11, v11, 1.0
	v_rcp_f32_e32 v26, v12
	v_div_scale_f32 v21, s[4:5], v11, v11, v10
	v_rcp_f32_e32 v27, v21
	v_fma_f32 v30, -v12, v26, 1.0
	s_waitcnt vmcnt(1)
	v_lshlrev_b32_e32 v19, 16, v13
	v_div_scale_f32 v13, vcc, 1.0, v11, 1.0
	v_fmac_f32_e32 v26, v30, v26
	v_mul_f32_e32 v30, v13, v26
	v_fma_f32 v31, -v21, v27, 1.0
	v_fma_f32 v33, -v12, v30, v13
	v_div_scale_f32 v22, s[4:5], v10, v11, v10
	v_fmac_f32_e32 v27, v31, v27
	v_fmac_f32_e32 v30, v33, v26
	v_mul_f32_e32 v31, v22, v27
	v_fma_f32 v12, -v12, v30, v13
	v_fma_f32 v34, -v21, v31, v22
	v_div_fmas_f32 v12, v12, v26, v30
	v_fmac_f32_e32 v31, v34, v27
	v_div_fixup_f32 v12, v12, v11, 1.0
	v_fma_f32 v13, -v21, v31, v22
	s_mov_b64 vcc, s[4:5]
	v_fma_f32 v12, v24, v12, v23
	v_div_fmas_f32 v13, v13, v27, v31
	v_cmp_gt_f32_e32 vcc, s74, v12
	v_add_f32_e32 v38, 1.0, v37
	v_div_scale_f32 v25, s[6:7], v38, v38, 1.0
	v_cndmask_b32_e64 v21, 0, 32, vcc
	v_ldexp_f32 v12, v12, v21
	v_log_f32_e32 v12, v12
	v_rcp_f32_e32 v28, v25
	v_div_fixup_f32 v10, v13, v11, v10
	v_div_scale_f32 v29, s[6:7], 1.0, v38, 1.0
	v_mul_f32_e32 v11, 0x3f317217, v12
	v_fma_f32 v11, v12, s75, -v11
	v_fma_f32 v32, -v25, v28, 1.0
	v_fmac_f32_e32 v11, 0x3377d1cf, v12
	v_fmac_f32_e32 v28, v32, v28
	v_mul_f32_e32 v21, v24, v10
	v_cndmask_b32_e32 v10, 0, v103, vcc
	v_fmac_f32_e32 v11, 0x3f317217, v12
	v_cmp_lt_f32_e64 vcc, |v12|, s76
	v_mul_f32_e32 v32, v29, v28
	v_fma_f32 v35, -v25, v32, v29
	v_cndmask_b32_e32 v11, v12, v11, vcc
	v_div_scale_f32 v12, s[4:5], v38, v38, v37
	v_rcp_f32_e32 v39, v12
	v_fmac_f32_e32 v32, v35, v28
	v_sub_f32_e32 v10, v11, v10
	v_add_f32_e32 v22, 0, v10
	v_fma_f32 v10, -v25, v32, v29
	s_mov_b64 vcc, s[6:7]
	v_div_fmas_f32 v10, v10, v28, v32
	v_div_fixup_f32 v13, v10, v38, 1.0
	v_fma_f32 v10, -v12, v39, 1.0
	v_fmac_f32_e32 v39, v10, v39
	v_div_scale_f32 v25, vcc, v37, v38, v37
	s_mov_b32 s4, 0xc000
	v_mul_f32_e32 v40, v25, v39
	v_add_co_u32_e64 v10, s[4:5], s4, v8
	v_fma_f32 v26, -v12, v40, v25
	s_nop 0
	v_addc_co_u32_e64 v11, s[4:5], 0, v9, s[4:5]
	v_fmac_f32_e32 v40, v26, v39
	s_mov_b32 s4, 0x10000
	v_fma_f32 v42, -v12, v40, v25
	v_add_co_u32_e64 v12, s[4:5], s4, v8
	global_load_ushort v41, v[10:11], off offset:-4096
	v_fma_f32 v43, v24, v13, v23
	v_addc_co_u32_e64 v13, s[4:5], 0, v9, s[4:5]
	v_add_co_u32_e64 v28, s[4:5], s35, v8
	s_mov_b64 s[6:7], 0x45c82000
	s_nop 0
	v_addc_co_u32_e64 v29, s[4:5], 0, v9, s[4:5]
	v_add_co_u32_e64 v26, s[4:5], s16, v8
	v_lshl_add_u64 v[6:7], v[6:7], 0, s[6:7]
	s_nop 0
	v_addc_co_u32_e64 v27, s[4:5], 0, v9, s[4:5]
	s_mov_b32 s4, 0x1b000
	s_nop 0
	v_add_co_u32_e64 v30, s[4:5], s4, v8
	s_movk_i32 s6, 0x880
	s_nop 0
	v_addc_co_u32_e64 v31, s[4:5], 0, v9, s[4:5]
	s_mov_b32 s4, 0x1c000
	s_nop 0
	v_add_co_u32_e64 v32, s[4:5], s4, v8
	s_waitcnt vmcnt(0)
; __device__ __forceinline__ float bf2f(bf16 b) { return __uint_as_float(((unsigned)b) << 16); }
; __device__ __forceinline__ void hgrn_x1_unit(const Args& a, int layer, int unit, LAS unsigned char* lds) {
;     ...
;     for (int i = 0; i < 8; ++i) {
;         const bf16* pr = PROJ + (tok0 + 8 * tq + i) * DIN + h * 128 + d;
;         q[i] = bf2f(pr[C_QA]); vv[i] = pr[C_IA];
;         float z = bf2f(pr[C_FA]); z = fminf(fmaxf(z, -30.f), 30.f);
;         const float e = __expf(-z), sp = 1.0f / (1.0f + e), sn = e / (1.0f + e);
;         const float f = lb + (1.0f - lb) * sp; kk[i] = (1.0f - lb) * sn;
;         run += __logf(f); c[i] = run;
;     }
	v_lshlrev_b32_e32 v54, 16, v41
	v_addc_co_u32_e64 v33, s[4:5], 0, v9, s[4:5]
	s_mov_b32 s4, 0x21000
	s_nop 0
	v_add_co_u32_e64 v34, s[4:5], s4, v8
	s_nop 1
	v_addc_co_u32_e64 v35, s[4:5], 0, v9, s[4:5]
	global_load_ushort v44, v[12:13], off offset:2048
	global_load_ushort v25, v[28:29], off offset:2048
	global_load_ushort v45, v[26:27], off offset:2048
	global_load_ushort v46, v[30:31], off offset:2048
	s_nop 0
	global_load_ushort v26, v[32:33], off offset:2048
	s_nop 0
	global_load_ushort v34, v[34:35], off offset:2048
	s_nop 0
	global_load_ushort v32, v[32:33], off
	s_nop 0
	global_load_ushort v33, v[28:29], off
	v_cmp_gt_f32_e64 s[4:5], s74, v43
	v_div_fmas_f32 v13, v42, v39, v40
	v_div_fixup_f32 v13, v13, v38, v37
	v_cndmask_b32_e64 v12, 0, 32, s[4:5]
	v_ldexp_f32 v12, v43, v12
	v_log_f32_e32 v12, v12
	v_mul_f32_e32 v52, v24, v13
	v_mul_f32_e32 v13, 0x3f317217, v12
	v_fma_f32 v13, v12, s75, -v13
	v_fmac_f32_e32 v13, 0x3377d1cf, v12
	v_fmac_f32_e32 v13, 0x3f317217, v12
	v_cmp_lt_f32_e64 vcc, |v12|, s76
	s_waitcnt vmcnt(7)
	v_lshlrev_b32_e32 v57, 16, v44
	v_cndmask_b32_e32 v12, v12, v13, vcc
	v_lshlrev_b32_e32 v13, 16, v36
	v_max_f32_e32 v13, v13, v13
	v_med3_f32 v13, v13, s73, v102
	v_mul_f32_e32 v13, 0xbfb8aa3b, v13
	v_exp_f32_e32 v35, v13
	v_cndmask_b32_e64 v13, 0, v103, s[4:5]
	v_add_co_u32_e32 v28, vcc, s17, v8
	v_add_f32_e32 v36, 1.0, v35
	v_div_scale_f32 v37, s[4:5], v36, v36, 1.0
	v_sub_f32_e32 v12, v12, v13
	v_addc_co_u32_e32 v29, vcc, 0, v9, vcc
	s_mov_b32 s4, 0x22000
	v_add_f32_e32 v53, v22, v12
	v_add_co_u32_e32 v12, vcc, s4, v8
	s_mov_b32 s4, 0x27000
	s_nop 0
	v_addc_co_u32_e32 v13, vcc, 0, v9, vcc
	v_add_co_u32_e32 v30, vcc, s4, v8
	v_rcp_f32_e32 v38, v37
	s_nop 0
	v_addc_co_u32_e32 v31, vcc, 0, v9, vcc
	global_load_ushort v10, v[10:11], off
	s_nop 0
	global_load_ushort v39, v[28:29], off offset:-4096
	global_load_ushort v11, v[28:29], off
	s_nop 0
	global_load_ushort v28, v[12:13], off offset:-4096
	global_load_ushort v27, v[30:31], off offset:2048
	v_fma_f32 v29, -v37, v38, 1.0
	v_fmac_f32_e32 v38, v29, v38
	v_div_scale_f32 v29, vcc, 1.0, v36, 1.0
	v_mul_f32_e32 v40, v29, v38
	v_fma_f32 v41, -v37, v40, v29
	v_fmac_f32_e32 v40, v41, v38
	v_fma_f32 v29, -v37, v40, v29
	v_div_scale_f32 v37, s[4:5], v36, v36, v35
	v_rcp_f32_e32 v41, v37
	v_div_fmas_f32 v29, v29, v38, v40
	v_div_fixup_f32 v29, v29, v36, 1.0
	v_fma_f32 v29, v24, v29, v23
	v_fma_f32 v38, -v37, v41, 1.0
	v_fmac_f32_e32 v41, v38, v41
	v_div_scale_f32 v38, vcc, v35, v36, v35
	v_mul_f32_e32 v40, v38, v41
	v_fma_f32 v42, -v37, v40, v38
	v_fmac_f32_e32 v40, v42, v41
	v_cmp_gt_f32_e64 s[4:5], s74, v29
	v_fma_f32 v37, -v37, v40, v38
	s_waitcnt vmcnt(5)
	v_lshlrev_b32_e32 v33, 16, v33
	v_cndmask_b32_e64 v38, 0, 32, s[4:5]
	v_ldexp_f32 v29, v29, v38
	v_log_f32_e32 v29, v29
	v_max_f32_e32 v33, v33, v33
	v_med3_f32 v33, v33, s73, v102
	v_div_fmas_f32 v37, v37, v41, v40
	v_mul_f32_e32 v33, 0xbfb8aa3b, v33
	v_div_fixup_f32 v35, v37, v36, v35
	v_exp_f32_e32 v33, v33
	v_mul_f32_e32 v55, v24, v35
	v_mul_f32_e32 v35, 0x3f317217, v29
	v_fma_f32 v35, v29, s75, -v35
	v_fmac_f32_e32 v35, 0x3377d1cf, v29
	v_fmac_f32_e32 v35, 0x3f317217, v29
	v_cmp_lt_f32_e64 vcc, |v29|, s76
	v_add_f32_e32 v36, 1.0, v33
	v_lshlrev_b32_e32 v32, 16, v32
	v_cndmask_b32_e32 v29, v29, v35, vcc
	v_cndmask_b32_e64 v35, 0, v103, s[4:5]
	v_div_scale_f32 v37, s[4:5], v36, v36, 1.0
	v_rcp_f32_e32 v38, v37
	v_sub_f32_e32 v29, v29, v35
	v_add_f32_e32 v56, v53, v29
	v_max_f32_e32 v32, v32, v32
	v_fma_f32 v29, -v37, v38, 1.0
	v_fmac_f32_e32 v38, v29, v38
	v_div_scale_f32 v29, vcc, 1.0, v36, 1.0
	v_mul_f32_e32 v35, v29, v38
	v_fma_f32 v40, -v37, v35, v29
	v_fmac_f32_e32 v35, v40, v38
	v_fma_f32 v29, -v37, v35, v29
	v_div_scale_f32 v37, s[4:5], v36, v36, v33
	v_rcp_f32_e32 v40, v37
	v_div_fmas_f32 v29, v29, v38, v35
	v_div_fixup_f32 v29, v29, v36, 1.0
	v_fma_f32 v29, v24, v29, v23
	v_fma_f32 v35, -v37, v40, 1.0
	v_fmac_f32_e32 v40, v35, v40
	v_div_scale_f32 v35, vcc, v33, v36, v33
	v_mul_f32_e32 v38, v35, v40
	v_fma_f32 v41, -v37, v38, v35
	v_fmac_f32_e32 v38, v41, v40
	v_fma_f32 v35, -v37, v38, v35
	v_cmp_gt_f32_e64 s[4:5], s74, v29
	v_div_fmas_f32 v35, v35, v40, v38
	v_div_fixup_f32 v33, v35, v36, v33
	v_cndmask_b32_e64 v37, 0, 32, s[4:5]
	v_ldexp_f32 v29, v29, v37
	v_lshlrev_b32_e32 v35, 16, v45
	v_log_f32_e32 v29, v29
	v_max_f32_e32 v35, v35, v35
	v_med3_f32 v35, v35, s73, v102
	v_mul_f32_e32 v35, 0xbfb8aa3b, v35
	v_exp_f32_e32 v35, v35
	v_mul_f32_e32 v58, v24, v33
	v_mul_f32_e32 v33, 0x3f317217, v29
	v_fma_f32 v33, v29, s75, -v33
	v_fmac_f32_e32 v33, 0x3377d1cf, v29
	v_fmac_f32_e32 v33, 0x3f317217, v29
	v_cmp_lt_f32_e64 vcc, |v29|, s76
	v_add_f32_e32 v36, 1.0, v35
	s_waitcnt vmcnt(3)
	v_lshlrev_b32_e32 v60, 16, v39
	v_cndmask_b32_e32 v29, v29, v33, vcc
	v_cndmask_b32_e64 v33, 0, v103, s[4:5]
	v_div_scale_f32 v37, s[4:5], v36, v36, 1.0
	v_rcp_f32_e32 v38, v37
	v_sub_f32_e32 v29, v29, v33
	v_add_f32_e32 v59, v56, v29
	v_med3_f32 v32, v32, s73, v102
	v_fma_f32 v29, -v37, v38, 1.0
	v_fmac_f32_e32 v38, v29, v38
	v_div_scale_f32 v29, vcc, 1.0, v36, 1.0
	v_mul_f32_e32 v33, v29, v38
	v_fma_f32 v39, -v37, v33, v29
	v_fmac_f32_e32 v33, v39, v38
	v_fma_f32 v29, -v37, v33, v29
	v_div_scale_f32 v37, s[4:5], v36, v36, v35
	v_rcp_f32_e32 v39, v37
	v_div_fmas_f32 v29, v29, v38, v33
	v_div_fixup_f32 v29, v29, v36, 1.0
	v_fma_f32 v29, v24, v29, v23
	v_fma_f32 v33, -v37, v39, 1.0
	v_fmac_f32_e32 v39, v33, v39
	v_div_scale_f32 v33, vcc, v35, v36, v35
	v_mul_f32_e32 v38, v33, v39
	v_fma_f32 v40, -v37, v38, v33
	v_fmac_f32_e32 v38, v40, v39
	v_cmp_gt_f32_e64 s[4:5], s74, v29
	v_fma_f32 v33, -v37, v38, v33
	v_div_fmas_f32 v33, v33, v39, v38
	v_cndmask_b32_e64 v37, 0, 32, s[4:5]
	v_ldexp_f32 v29, v29, v37
	v_log_f32_e32 v29, v29
	v_mul_f32_e32 v32, 0xbfb8aa3b, v32
	v_div_fixup_f32 v33, v33, v36, v35
	v_exp_f32_e32 v32, v32
	v_mul_f32_e32 v61, v24, v33
	v_mul_f32_e32 v33, 0x3f317217, v29
	v_fma_f32 v33, v29, s75, -v33
	v_fmac_f32_e32 v33, 0x3377d1cf, v29
	v_fmac_f32_e32 v33, 0x3f317217, v29
	v_cmp_lt_f32_e64 vcc, |v29|, s76
	v_add_f32_e32 v35, 1.0, v32
	s_waitcnt vmcnt(1)
; __device__ __forceinline__ float bf2f(bf16 b) { return __uint_as_float(((unsigned)b) << 16); }
; __device__ __forceinline__ void hgrn_x1_unit(const Args& a, int layer, int unit, LAS unsigned char* lds) {
;     ...
;     for (int i = 0; i < 8; ++i) {
;         const bf16* pr = PROJ + (tok0 + 8 * tq + i) * DIN + h * 128 + d;
;         q[i] = bf2f(pr[C_QA]); vv[i] = pr[C_IA];
;         float z = bf2f(pr[C_FA]); z = fminf(fmaxf(z, -30.f), 30.f);
;         const float e = __expf(-z), sp = 1.0f / (1.0f + e), sn = e / (1.0f + e);
;         const float f = lb + (1.0f - lb) * sp; kk[i] = (1.0f - lb) * sn;
;         run += __logf(f); c[i] = run;
;     }
;     __syncthreads();
;     TOT[tq * 128 + d] = run;
;     __syncthreads();
	v_lshlrev_b32_e32 v66, 16, v28
	v_cndmask_b32_e32 v29, v29, v33, vcc
	v_cndmask_b32_e64 v33, 0, v103, s[4:5]
	v_div_scale_f32 v36, s[4:5], v35, v35, 1.0
	s_mov_b32 s4, 0x26000
	s_nop 0
	v_add_co_u32_e64 v8, s[4:5], s4, v8
	v_rcp_f32_e32 v37, v36
	s_nop 0
	v_addc_co_u32_e64 v9, s[4:5], 0, v9, s[4:5]
	global_load_ushort v8, v[8:9], off offset:2048
	s_nop 0
	global_load_ushort v9, v[30:31], off
	v_sub_f32_e32 v29, v29, v33
	v_add_f32_e32 v62, v59, v29
	v_fma_f32 v29, -v36, v37, 1.0
	v_fmac_f32_e32 v37, v29, v37
	v_div_scale_f32 v29, vcc, 1.0, v35, 1.0
	v_div_scale_f32 v30, s[4:5], v35, v35, v32
	v_mul_f32_e32 v33, v29, v37
	v_rcp_f32_e32 v31, v30
	v_fma_f32 v38, -v36, v33, v29
	v_fmac_f32_e32 v33, v38, v37
	v_fma_f32 v29, -v36, v33, v29
	v_div_fmas_f32 v29, v29, v37, v33
	v_fma_f32 v33, -v30, v31, 1.0
	v_fmac_f32_e32 v31, v33, v31
	v_div_scale_f32 v33, vcc, v32, v35, v32
	v_div_fixup_f32 v29, v29, v35, 1.0
	v_mul_f32_e32 v36, v33, v31
	v_fma_f32 v37, -v30, v36, v33
	v_fma_f32 v29, v24, v29, v23
	v_fmac_f32_e32 v36, v37, v31
	v_cmp_gt_f32_e64 s[4:5], s74, v29
	v_fma_f32 v30, -v30, v36, v33
	v_div_fmas_f32 v30, v30, v31, v36
	v_cndmask_b32_e64 v33, 0, 32, s[4:5]
	v_ldexp_f32 v29, v29, v33
	v_log_f32_e32 v29, v29
	v_lshlrev_b32_e32 v31, 16, v34
	v_max_f32_e32 v31, v31, v31
	v_div_fixup_f32 v30, v30, v35, v32
	v_med3_f32 v31, v31, s73, v102
	v_mul_f32_e32 v64, v24, v30
	v_mul_f32_e32 v30, 0x3f317217, v29
	v_mul_f32_e32 v31, 0xbfb8aa3b, v31
	v_fma_f32 v30, v29, s75, -v30
	v_exp_f32_e32 v31, v31
	v_fmac_f32_e32 v30, 0x3377d1cf, v29
	v_fmac_f32_e32 v30, 0x3f317217, v29
	v_cmp_lt_f32_e64 vcc, |v29|, s76
	global_load_ushort v67, v[12:13], off
	s_nop 0
	v_cndmask_b32_e32 v29, v29, v30, vcc
	v_cndmask_b32_e64 v30, 0, v103, s[4:5]
	v_sub_f32_e32 v29, v29, v30
	v_add_f32_e32 v30, 1.0, v31
	v_div_scale_f32 v32, s[4:5], v30, v30, 1.0
	v_rcp_f32_e32 v33, v32
	v_add_f32_e32 v65, v62, v29
	s_barrier
	v_fma_f32 v12, -v32, v33, 1.0
	v_fmac_f32_e32 v33, v12, v33
	v_div_scale_f32 v12, vcc, 1.0, v30, 1.0
	v_mul_f32_e32 v13, v12, v33
	v_fma_f32 v28, -v32, v13, v12
	v_fmac_f32_e32 v13, v28, v33
	v_div_scale_f32 v28, s[4:5], v30, v30, v31
	v_rcp_f32_e32 v29, v28
	v_fma_f32 v12, -v32, v13, v12
	v_div_fmas_f32 v12, v12, v33, v13
	v_div_fixup_f32 v12, v12, v30, 1.0
	v_fma_f32 v13, -v28, v29, 1.0
	v_fmac_f32_e32 v29, v13, v29
	v_div_scale_f32 v13, vcc, v31, v30, v31
	v_mul_f32_e32 v32, v13, v29
	v_fma_f32 v33, -v28, v32, v13
	v_fma_f32 v12, v24, v12, v23
	v_fmac_f32_e32 v32, v33, v29
	v_cmp_gt_f32_e64 s[4:5], s74, v12
	v_fma_f32 v13, -v28, v32, v13
	v_div_fmas_f32 v13, v13, v29, v32
	v_cndmask_b32_e64 v28, 0, 32, s[4:5]
	v_ldexp_f32 v12, v12, v28
	s_waitcnt vmcnt(1)
	v_lshlrev_b32_e32 v9, 16, v9
	v_log_f32_e32 v12, v12
	v_max_f32_e32 v9, v9, v9
	v_med3_f32 v9, v9, s73, v102
	v_mul_f32_e32 v9, 0xbfb8aa3b, v9
	v_div_fixup_f32 v13, v13, v30, v31
	v_exp_f32_e32 v9, v9
	v_mul_f32_e32 v68, v24, v13
	v_mul_f32_e32 v13, 0x3f317217, v12
	v_fma_f32 v13, v12, s75, -v13
	v_fmac_f32_e32 v13, 0x3377d1cf, v12
	v_fmac_f32_e32 v13, 0x3f317217, v12
	v_cmp_lt_f32_e64 vcc, |v12|, s76
	v_add_f32_e32 v28, 1.0, v9
	v_lshlrev_b32_e32 v70, 16, v8
	v_cndmask_b32_e32 v12, v12, v13, vcc
	v_cndmask_b32_e64 v13, 0, v103, s[4:5]
	v_div_scale_f32 v29, s[4:5], v28, v28, 1.0
	v_rcp_f32_e32 v30, v29
	v_sub_f32_e32 v12, v12, v13
	v_add_f32_e32 v69, v65, v12
	v_lshl_add_u64 v[36:37], v[6:7], 0, v[4:5]
	v_fma_f32 v8, -v29, v30, 1.0
	v_fmac_f32_e32 v30, v8, v30
	v_div_scale_f32 v8, vcc, 1.0, v28, 1.0
	v_mul_f32_e32 v12, v8, v30
	v_fma_f32 v13, -v29, v12, v8
	v_fmac_f32_e32 v12, v13, v30
	v_div_scale_f32 v13, s[4:5], v28, v28, v9
	v_fma_f32 v8, -v29, v12, v8
	v_rcp_f32_e32 v29, v13
	v_div_fmas_f32 v8, v8, v30, v12
	v_div_fixup_f32 v8, v8, v28, 1.0
	v_fmac_f32_e32 v23, v24, v8
	v_fma_f32 v12, -v13, v29, 1.0
	v_cmp_gt_f32_e64 s[4:5], s74, v23
	v_fmac_f32_e32 v29, v12, v29
	v_div_scale_f32 v12, vcc, v9, v28, v9
	v_cndmask_b32_e64 v8, 0, 32, s[4:5]
	v_mul_f32_e32 v30, v12, v29
	v_ldexp_f32 v8, v23, v8
	v_fma_f32 v31, -v13, v30, v12
	v_log_f32_e32 v8, v8
	v_fmac_f32_e32 v30, v31, v29
	v_fma_f32 v12, -v13, v30, v12
	v_div_fmas_f32 v12, v12, v29, v30
	v_div_fixup_f32 v23, v12, v28, v9
	v_mul_f32_e32 v9, 0x3f317217, v8
	v_fma_f32 v9, v8, s75, -v9
	v_fmac_f32_e32 v9, 0x3377d1cf, v8
	v_fmac_f32_e32 v9, 0x3f317217, v8
	v_cmp_lt_f32_e64 vcc, |v8|, s76
	v_or_b32_e32 v4, 1, v2
	v_ashrrev_i32_e32 v5, 31, v4
	v_cndmask_b32_e32 v8, v8, v9, vcc
	v_cndmask_b32_e64 v9, 0, v103, s[4:5]
	v_sub_f32_e32 v8, v8, v9
	v_add_f32_e32 v9, v69, v8
	v_lshl_add_u32 v8, v14, 2, 0
	ds_write_b32 v8, v9
	v_lshl_add_u32 v8, v15, 2, 0
	s_waitcnt lgkmcnt(0)
	s_barrier
; #define LAS __attribute__((address_space(3)))
; __device__ __forceinline__ bf16 f2bf(float f) { return (bf16)(pk2(f, 0.f) & 0xffffu); }
; __device__ __forceinline__ void hgrn_x1_unit(const Args& a, int layer, int unit, LAS unsigned char* lds) {
;     ...
;     float off = 0.f, bl = 0.f;
; #pragma unroll
;     for (int g = 0; g < 4; ++g) { const float t = TOT[g * 128 + d]; bl += t; off += (g < tq) ? t : 0.f; }
;     unsigned kh[8];
; #pragma unroll
;     for (int i = 0; i < 8; ++i) {
;         const float bt = off + c[i];
;         const float qt = q[i] * __expf(bt), kh_ = kk[i] * __expf(bl - bt), kp = kk[i] * __expf(fminf(-bt, 80.f));
;         const int t = 8 * tq + i;
;         const bf16 qb = f2bf(qt);
;         *(LAS bf16*)(lds + HX_QL + t * 272 + d * 2) = qb;
;         *(LAS bf16*)(lds + HX_KP + t * 272 + d * 2) = f2bf(kp);
;         QT[(tok0 + t) * 1024 + h * 128 + d] = qb;
;         kh[i] = f2bf(kh_);
;     }
;     { u32x4 o; o.x = kh[0] | (kh[1] << 16); o.y = kh[2] | (kh[3] << 16); o.z = kh[4] | (kh[5] << 16); o.w = kh[6] | (kh[7] << 16); *(u32x4*)(KT + d * 32 + 8 * tq) = o;
	ds_read2st64_b32 v[12:13], v8 offset1:2
	ds_read2st64_b32 v[28:29], v8 offset0:4 offset1:6
	v_sub_u32_e32 v8, v8, v82
	v_mad_u64_u32 v[34:35], s[6:7], v16, s6, v[8:9]
	s_movk_i32 s6, 0x110
	s_nop 0
	v_mad_u64_u32 v[38:39], s[6:7], v4, s6, v[8:9]
	v_lshl_add_u64 v[4:5], v[4:5], 0, s[10:11]
	v_lshlrev_b64 v[4:5], 11, v[4:5]
	v_lshl_add_u64 v[40:41], v[6:7], 0, v[4:5]
	v_or_b32_e32 v4, 2, v2
	v_ashrrev_i32_e32 v5, 31, v4
	v_lshl_add_u64 v[4:5], v[4:5], 0, s[10:11]
	v_lshlrev_b64 v[4:5], 11, v[4:5]
	v_lshl_add_u64 v[42:43], v[6:7], 0, v[4:5]
	v_or_b32_e32 v4, 3, v2
	v_ashrrev_i32_e32 v5, 31, v4
	v_lshl_add_u64 v[4:5], v[4:5], 0, s[10:11]
	v_lshlrev_b64 v[4:5], 11, v[4:5]
	v_lshl_add_u64 v[44:45], v[6:7], 0, v[4:5]
	v_or_b32_e32 v4, 4, v2
	v_ashrrev_i32_e32 v5, 31, v4
	v_lshl_add_u64 v[4:5], v[4:5], 0, s[10:11]
	v_lshlrev_b64 v[4:5], 11, v[4:5]
	v_lshlrev_b32_e32 v63, 16, v46
	v_lshl_add_u64 v[46:47], v[6:7], 0, v[4:5]
	v_or_b32_e32 v4, 5, v2
	v_ashrrev_i32_e32 v5, 31, v4
	v_lshl_add_u64 v[4:5], v[4:5], 0, s[10:11]
	v_lshlrev_b64 v[4:5], 11, v[4:5]
	v_cmp_lt_i32_e32 vcc, 1, v16
	v_lshl_add_u64 v[48:49], v[6:7], 0, v[4:5]
	v_or_b32_e32 v4, 6, v2
	v_mul_f32_e32 v23, v24, v23
	s_waitcnt lgkmcnt(1)
	v_cndmask_b32_e32 v24, 0, v13, vcc
	v_cmp_lt_i32_e32 vcc, 2, v16
	v_ashrrev_i32_e32 v5, 31, v4
	v_lshl_add_u64 v[4:5], v[4:5], 0, s[10:11]
	s_waitcnt lgkmcnt(0)
	v_cndmask_b32_e32 v31, 0, v28, vcc
	v_cmp_lt_i32_e32 vcc, 3, v16
	v_lshlrev_b64 v[50:51], 11, v[4:5]
	v_add_f32_e32 v4, 0, v12
	v_cndmask_b32_e32 v33, 0, v29, vcc
	v_cmp_lt_i32_e32 vcc, 0, v16
	v_mov_b32_e32 v30, v13
	v_mov_b32_e32 v32, v28
	v_cndmask_b32_e32 v5, 0, v4, vcc
	v_add_f32_e32 v5, v5, v24
	v_pk_add_f32 v[4:5], v[4:5], v[30:31]
	v_mov_b32_e32 v8, v29
	v_pk_add_f32 v[12:13], v[4:5], v[32:33]
	s_lshl_b64 s[4:5], s[22:23], 13
	v_add_f32_e32 v22, v22, v13
	v_mul_f32_e32 v4, 0x3fb8aa3b, v22
	v_exp_f32_e32 v24, v4
	v_pk_add_f32 v[4:5], v[12:13], v[8:9]
	s_add_u32 s4, s8, s4
	v_sub_f32_e32 v8, v4, v22
	v_mul_f32_e32 v8, 0x3fb8aa3b, v8
	v_exp_f32_e32 v12, v8
	v_min_f32_e64 v8, -v22, s89
	v_mul_f32_e32 v8, 0x3fb8aa3b, v8
	v_exp_f32_e32 v22, v8
	v_mul_f32_e32 v20, v24, v20
	v_mul_f32_e32 v12, v21, v12
	v_cvt_pk_bf16_f32 v20, v20, v83
	v_mul_f32_e32 v21, v21, v22
	ds_write_b16 v34, v20 offset:2048
	v_cvt_pk_bf16_f32 v21, v21, v83
	s_nop 0
	v_add_f32_e32 v20, v53, v13
	ds_write_b16 v34, v21 offset:10752
	v_mul_f32_e32 v21, 0x3fb8aa3b, v20
	v_sub_f32_e32 v22, v4, v20
	v_min_f32_e64 v20, -v20, s89
	v_exp_f32_e32 v21, v21
	v_mul_f32_e32 v20, 0x3fb8aa3b, v20
	v_exp_f32_e32 v20, v20
	v_mul_f32_e32 v22, 0x3fb8aa3b, v22
	v_exp_f32_e32 v22, v22
	v_mul_f32_e32 v19, v21, v19
	v_cvt_pk_bf16_f32 v12, v12, v83
	v_mul_f32_e32 v20, v52, v20
	v_cvt_pk_bf16_f32 v19, v19, v83
	ds_write_b16 v38, v19 offset:2048
	v_cvt_pk_bf16_f32 v20, v20, v83
	s_nop 0
	v_add_f32_e32 v19, v56, v13
	v_mul_f32_e32 v21, v52, v22
	ds_write_b16 v38, v20 offset:10752
	v_mul_f32_e32 v20, 0x3fb8aa3b, v19
	v_sub_f32_e32 v22, v4, v19
	v_min_f32_e64 v19, -v19, s89
	v_exp_f32_e32 v20, v20
	v_mul_f32_e32 v19, 0x3fb8aa3b, v19
	v_mul_f32_e32 v22, 0x3fb8aa3b, v22
	v_exp_f32_e32 v19, v19
	v_exp_f32_e32 v22, v22
	v_mul_f32_e32 v20, v20, v54
	v_cvt_pk_bf16_f32 v21, v21, v83
	v_mul_f32_e32 v19, v55, v19
	v_cvt_pk_bf16_f32 v20, v20, v83
	v_mul_f32_e32 v22, v55, v22
	ds_write_b16 v38, v20 offset:2320
	v_cvt_pk_bf16_f32 v19, v19, v83
	s_nop 0
	v_add_f32_e32 v20, v59, v13
	ds_write_b16 v38, v19 offset:11024
	v_cvt_pk_bf16_f32 v19, v22, v83
	v_mul_f32_e32 v22, 0x3fb8aa3b, v20
	v_sub_f32_e32 v24, v4, v20
	v_min_f32_e64 v20, -v20, s89
	v_mul_f32_e32 v20, 0x3fb8aa3b, v20
	v_exp_f32_e32 v22, v22
	v_exp_f32_e32 v20, v20
	v_mul_f32_e32 v24, 0x3fb8aa3b, v24
	v_exp_f32_e32 v24, v24
	v_mul_f32_e32 v22, v22, v57
	v_mul_f32_e32 v20, v58, v20
	v_cvt_pk_bf16_f32 v22, v22, v83
	ds_write_b16 v38, v22 offset:2592
	v_cvt_pk_bf16_f32 v20, v20, v83
	ds_write_b16 v38, v20 offset:11296
	v_add_f32_e32 v20, v62, v13
	s_nop 0
	v_mul_f32_e32 v22, 0x3fb8aa3b, v20
	v_sub_f32_e32 v28, v4, v20
	v_min_f32_e64 v20, -v20, s89
	v_exp_f32_e32 v22, v22
	v_mul_f32_e32 v20, 0x3fb8aa3b, v20
	v_mul_f32_e32 v28, 0x3fb8aa3b, v28
	v_exp_f32_e32 v20, v20
	v_exp_f32_e32 v28, v28
	v_mul_f32_e32 v24, v58, v24
	v_mul_f32_e32 v22, v22, v60
	v_cvt_pk_bf16_f32 v24, v24, v83
	v_mul_f32_e32 v20, v61, v20
	v_cvt_pk_bf16_f32 v22, v22, v83
	v_mul_f32_e32 v28, v61, v28
	ds_write_b16 v38, v22 offset:2864
	v_cvt_pk_bf16_f32 v20, v20, v83
	s_nop 0
	v_add_f32_e32 v22, v65, v13
	ds_write_b16 v38, v20 offset:11568
	v_cvt_pk_bf16_f32 v20, v28, v83
	v_mul_f32_e32 v28, 0x3fb8aa3b, v22
	v_sub_f32_e32 v29, v4, v22
	v_min_f32_e64 v22, -v22, s89
	v_mul_f32_e32 v22, 0x3fb8aa3b, v22
	v_exp_f32_e32 v28, v28
	v_exp_f32_e32 v22, v22
	v_add_f32_e32 v13, v69, v13
	v_mul_f32_e32 v29, 0x3fb8aa3b, v29
	v_mul_f32_e32 v28, v28, v63
	v_mul_f32_e32 v22, v64, v22
	v_cvt_pk_bf16_f32 v28, v28, v83
	ds_write_b16 v38, v28 offset:3136
	v_cvt_pk_bf16_f32 v22, v22, v83
	ds_write_b16 v38, v22 offset:11840
	s_nop 0
	v_mul_f32_e32 v22, 0x3fb8aa3b, v13
	v_sub_f32_e32 v28, v4, v13
	v_min_f32_e64 v13, -v13, s89
	v_mul_f32_e32 v13, 0x3fb8aa3b, v13
	v_exp_f32_e32 v29, v29
	v_exp_f32_e32 v22, v22
	v_exp_f32_e32 v13, v13
	v_lshl_add_u64 v[8:9], v[6:7], 0, v[50:51]
	v_mul_f32_e32 v29, v64, v29
	v_mul_f32_e32 v22, v22, v66
	v_mul_f32_e32 v13, v68, v13
	v_mul_f32_e32 v28, 0x3fb8aa3b, v28
	v_cvt_pk_bf16_f32 v29, v29, v83
	v_cvt_pk_bf16_f32 v22, v22, v83
	ds_write_b16 v38, v22 offset:3408
	v_cvt_pk_bf16_f32 v13, v13, v83
	v_exp_f32_e32 v28, v28
	ds_write_b16 v38, v13 offset:12112
	s_nop 0
	v_mul_f32_e32 v9, 0x3fb8aa3b, v5
	v_sub_f32_e32 v13, v4, v5
	v_min_f32_e64 v5, -v5, s89
	v_exp_f32_e32 v9, v9
	v_mul_f32_e32 v13, 0x3fb8aa3b, v13
	v_mul_f32_e32 v5, 0x3fb8aa3b, v5
	v_exp_f32_e32 v13, v13
	v_exp_f32_e32 v5, v5
	v_mul_f32_e32 v28, v68, v28
	v_cvt_pk_bf16_f32 v8, v28, v83
	v_mul_f32_e32 v9, v9, v70
	v_and_b32_e32 v22, 0xffff, v8
	v_or_b32_e32 v8, 7, v2
	v_mul_f32_e32 v13, v23, v13
	v_mul_f32_e32 v5, v23, v5
	v_cvt_pk_bf16_f32 v23, v9, v83
	v_ashrrev_i32_e32 v9, 31, v8
	v_lshl_add_u64 v[8:9], v[8:9], 0, s[10:11]
	v_lshlrev_b64 v[8:9], 11, v[8:9]
	s_addc_u32 s5, s9, s5
	v_and_b32_e32 v19, 0xffff, v19
	v_lshl_add_u64 v[6:7], v[6:7], 0, v[8:9]
	v_lshlrev_b32_e32 v82, 6, v15
	ds_write_b16 v38, v23 offset:3680
	v_cvt_pk_bf16_f32 v5, v5, v83
	s_nop 0
	v_perm_b32 v8, v26, v11, s90
	v_perm_b32 v6, v17, v18, s90
	v_lshl_or_b32 v11, v24, 16, v19
	v_lshl_add_u64 v[18:19], s[4:5], 0, v[82:83]
	v_lshl_add_u64 v[2:3], v[2:3], 1, v[18:19]
	v_add_co_u32_e32 v18, vcc, s91, v2
	s_waitcnt vmcnt(0)
; #define LAS __attribute__((address_space(3)))
; __device__ __forceinline__ unsigned pk2(float lo, float hi) { unsigned r; asm volatile("v_cvt_pk_bf16_f32 %0, %1, %2" : "=v"(r) : "v"(lo), "v"(hi)); return r; }
; __device__ __forceinline__ f32x4 mfma16(bf16x8 a, bf16x8 b, f32x4 c) { return __builtin_amdgcn_mfma_f32_16x16x32_bf16(a, b, c, 0, 0, 0); }
; __device__ __forceinline__ void hgrn_x1_unit(const Args& a, int layer, int unit, LAS unsigned char* lds) {
;     ...
;         QT[(tok0 + t) * 1024 + h * 128 + d] = qb;
;     ...
;     { u32x4 o; o.x = kh[0] | (kh[1] << 16); o.y = kh[2] | (kh[3] << 16); o.z = kh[4] | (kh[5] << 16); o.w = kh[6] | (kh[7] << 16); *(u32x4*)(KT + d * 32 + 8 * tq) = o;
;       u32x4 w; w.x = vv[0] | ((unsigned)vv[1] << 16); w.y = vv[2] | ((unsigned)vv[3] << 16); w.z = vv[4] | ((unsigned)vv[5] << 16); w.w = vv[6] | ((unsigned)vv[7] << 16);
;       *(u32x4*)(VT + d * 32 + 8 * tq) = w; *(LAS u32x4*)(lds + HX_VL + d * 80 + 16 * tq) = w; }
;     if (tq == 0) DEC[d] = __expf(bl);
;     __syncthreads();
;     const int fr = lane & 15, fg = lane >> 4, tt = wave & 1, vp = wave >> 1;
;     f32x4 sc[2];
; #pragma unroll
;     for (int st = 0; st < 2; ++st) { f32x4 acc = (f32x4){0.f, 0.f, 0.f, 0.f};
; #pragma unroll
;         for (int ks = 0; ks < 4; ++ks) {
;             const bf16x8 A = *(const LAS bf16x8*)(lds + HX_KP + (16 * st + fr) * 272 + (32 * ks + 8 * fg) * 2);
;             const bf16x8 B = *(const LAS bf16x8*)(lds + HX_QL + (16 * tt + fr) * 272 + (32 * ks + 8 * fg) * 2);
;             acc = mfma16(A, B, acc); }
; #pragma unroll
;         for (int r = 0; r < 4; ++r) acc[r] = (16 * st + 4 * fg + r <= 16 * tt + fr) ? acc[r] : 0.f;
;         sc[st] = acc; }
;     FragU P; P.u.x = pk2(sc[0][0], sc[0][1]); P.u.y = pk2(sc[0][2], sc[0][3]); P.u.z = pk2(sc[1][0], sc[1][1]); P.u.w = pk2(sc[1][2], sc[1][3]);
; #pragma unroll
;     for (int vi = 0; vi < 2; ++vi) { const int vt = 2 * vp + vi;
;         FragU V; V.h[0] = *(const LAS u32x2*)(lds + HX_VL + (16 * vt + fr) * 80 + (4 * fg) * 2); V.h[1] = *(const LAS u32x2*)(lds + HX_VL + (16 * vt + fr) * 80 + (16 + 4 * fg) * 2);
;         const f32x4 o = mfma16(P.v, V.v, (f32x4){0.f, 0.f, 0.f, 0.f});
; #pragma unroll
;         for (int r = 0; r < 4; ++r) OI[(tok0 + 16 * tt + 4 * fg + r) * 1024 + h * 128 + 16 * vt + fr] = o[r]; }
	v_perm_b32 v9, v27, v67, s90
	v_addc_co_u32_e32 v19, vcc, 0, v3, vcc
	v_add_co_u32_e32 v2, vcc, 0x47c82000, v2
	v_perm_b32 v7, v25, v10, s90
	s_nop 0
	v_addc_co_u32_e32 v3, vcc, 0, v3, vcc
	v_and_b32_e32 v12, 0xffff, v12
	v_and_b32_e32 v20, 0xffff, v20
	ds_write_b16 v38, v5 offset:12384
	v_cvt_pk_bf16_f32 v5, v13, v83
	global_store_dwordx4 v[2:3], v[6:9], off
	v_mul_u32_u24_e32 v2, 0x50, v15
	v_lshlrev_b32_e32 v3, 4, v16
	v_lshl_or_b32 v10, v21, 16, v12
	v_lshl_or_b32 v12, v29, 16, v20
	v_lshl_or_b32 v13, v5, 16, v22
	v_add3_u32 v2, 0, v2, v3
	v_cmp_gt_u32_e32 vcc, s93, v14
	global_store_dwordx4 v[18:19], v[10:13], off
	ds_write_b128 v2, v[6:9] offset:19456
	s_and_saveexec_b64 s[4:5], vcc
	s_cbranch_execz .LBB0_326
	s_lshl_b64 s[6:7], s[22:23], 9
	s_add_u32 s6, s8, s6
	v_mul_f32_e32 v4, 0x3fb8aa3b, v4
	s_addc_u32 s7, s9, s7
	v_lshlrev_b32_e32 v82, 2, v15
	v_exp_f32_e32 v4, v4
	v_lshl_add_u64 v[2:3], s[6:7], 0, v[82:83]
	v_add_co_u32_e32 v2, vcc, 0x48c82000, v2
	s_nop 1
	v_addc_co_u32_e32 v3, vcc, 0, v3, vcc
	global_store_dword v[2:3], v4, off
.LBB0_326:
	s_or_b64 exec, exec, s[4:5]
	v_and_b32_e32 v34, 15, v14
	v_bfe_u32 v35, v14, 4, 2
	v_lshlrev_b32_e32 v6, 4, v35
	v_mul_u32_u24_e32 v2, 0x110, v34
	v_add3_u32 v37, 0, v2, v6
	s_waitcnt lgkmcnt(0)
	s_barrier
	v_lshrrev_b32_e32 v241, 6, v0
	v_and_b32_e32 v242, 63, v0
	v_and_b32_e32 v240, 15, v242
	v_lshrrev_b32_e32 v243, 2, v241
	v_lshl_or_b32 v240, v243, 4, v240
	v_mul_u32_u24_e32 v240, 0x110, v240
	v_and_b32_e32 v243, 3, v241
	v_lshl_add_u32 v240, v243, 6, v240
	v_lshrrev_b32_e32 v243, 4, v242
	v_lshl_add_u32 v240, v243, 3, v240
	ds_read_b64 v[244:245], v240 offset:2048
	ds_read_b64 v[246:247], v240 offset:2080
	v_lshlrev_b32_e32 v248, 4, v0
	v_mov_b32_e32 v249, s22
	v_lshl_add_u32 v248, v249, 13, v248
	v_add_u32_e32 v248, 0x45c82000, v248
	v_mov_b32_e32 v249, 0
	v_lshl_add_u64 v[248:249], s[8:9], 0, v[248:249]
	s_waitcnt lgkmcnt(0)
	global_store_dwordx4 v[248:249], v[244:247], off
	ds_read_b128 v[2:5], v37 offset:10752
	s_lshr_b32 s4, s13, 2
	s_and_b32 s5, s4, 16
	v_or_b32_e32 v36, s5, v34
	v_mul_u32_u24_e32 v7, 0x110, v36
	v_add3_u32 v26, 0, v7, v6
	ds_read_b128 v[6:9], v37 offset:10816
	ds_read_b128 v[10:13], v26 offset:2048
	ds_read_b128 v[14:17], v26 offset:2112
	ds_read_b128 v[18:21], v37 offset:10880
	s_waitcnt lgkmcnt(2)
	v_mfma_f32_16x16x32_bf16 v[2:5], v[2:5], v[10:13], 0
	v_lshlrev_b32_e32 v38, 2, v35
	v_cmp_le_u32_e32 vcc, v38, v36
	s_ashr_i32 s4, s13, 2
	s_waitcnt lgkmcnt(1)
	v_mfma_f32_16x16x32_bf16 v[2:5], v[6:9], v[14:17], v[2:5]
	ds_read_b128 v[6:9], v37 offset:10944
	ds_read_b128 v[22:25], v26 offset:2176
	ds_read_b128 v[26:29], v26 offset:2240
	ds_read_b128 v[30:33], v37 offset:15168
	s_andn2_b32 s4, s4, 31
	s_waitcnt lgkmcnt(2)
	v_mfma_f32_16x16x32_bf16 v[2:5], v[18:21], v[22:25], v[2:5]
	ds_read_b128 v[18:21], v37 offset:15104
	v_lshlrev_b32_e32 v82, 2, v34
	s_waitcnt lgkmcnt(2)
	v_mfma_f32_16x16x32_bf16 v[2:5], v[6:9], v[26:29], v[2:5]
	ds_read_b128 v[6:9], v37 offset:15232
	s_waitcnt lgkmcnt(1)
	v_mfma_f32_16x16x32_bf16 v[10:13], v[18:21], v[10:13], 0
	ds_read_b128 v[18:21], v37 offset:15296
	s_nop 3
	v_cndmask_b32_e32 v39, 0, v2, vcc
	v_cmp_lt_u32_e32 vcc, v38, v36
	v_mfma_f32_16x16x32_bf16 v[10:13], v[30:33], v[14:17], v[10:13]
	v_or_b32_e32 v2, 2, v38
	v_cndmask_b32_e32 v40, 0, v3, vcc
	v_cmp_le_u32_e32 vcc, v2, v36
	s_waitcnt lgkmcnt(1)
	v_mfma_f32_16x16x32_bf16 v[6:9], v[6:9], v[22:25], v[10:13]
	v_or_b32_e32 v2, 3, v38
	v_cndmask_b32_e32 v14, 0, v4, vcc
	v_cmp_le_u32_e32 vcc, v2, v36
	v_or_b32_e32 v11, s4, v34
	v_or_b32_e32 v12, s5, v38
	v_cndmask_b32_e32 v10, 0, v5, vcc
	s_waitcnt lgkmcnt(0)
	v_mfma_f32_16x16x32_bf16 v[2:5], v[18:21], v[26:29], v[6:9]
	v_or_b32_e32 v18, s10, v12
	v_lshl_add_u64 v[12:13], s[8:9], 0, v[82:83]
	s_ashr_i32 s5, s4, 31
	v_or_b32_e32 v6, 16, v38
	v_cmp_le_u32_e32 vcc, v6, v36
	v_lshl_or_b32 v22, v18, 10, s12
	v_lshlrev_b32_e32 v82, 2, v22
	s_nop 0
	v_cndmask_b32_e32 v6, 0, v2, vcc
	v_or_b32_e32 v2, 17, v38
	v_cmp_le_u32_e32 vcc, v2, v36
	v_or_b32_e32 v2, 18, v38
	s_nop 0
	v_cndmask_b32_e32 v7, 0, v3, vcc
	v_cmp_le_u32_e32 vcc, v2, v36
	v_or_b32_e32 v2, 19, v38
	s_nop 0
	v_cndmask_b32_e32 v8, 0, v4, vcc
	v_cmp_le_u32_e32 vcc, v2, v36
	v_cvt_pk_bf16_f32 v2, v39, v40
	v_cvt_pk_bf16_f32 v3, v14, v10
	v_lshl_add_u32 v10, v35, 3, 0
	v_cvt_pk_bf16_f32 v4, v6, v7
	v_mad_u64_u32 v[6:7], s[6:7], v11, s92, v[10:11]
	v_cndmask_b32_e32 v5, 0, v5, vcc
	v_add_u32_e32 v6, 0x4800, v6
	v_cvt_pk_bf16_f32 v5, v8, v5
	ds_read2_b64 v[6:9], v6 offset0:128 offset1:132
	v_lshl_add_u64 v[14:15], s[4:5], 2, v[12:13]
	s_waitcnt lgkmcnt(0)
	v_mfma_f32_16x16x32_bf16 v[6:9], v[2:5], v[6:9], 0
	v_lshl_add_u64 v[16:17], v[14:15], 0, s[40:41]
	v_lshl_add_u64 v[18:19], v[16:17], 0, v[82:83]
	v_or_b32_e32 v82, 0x400, v22
	v_lshlrev_b64 v[20:21], 2, v[82:83]
	v_lshl_add_u64 v[12:13], v[16:17], 0, v[20:21]
	v_or_b32_e32 v82, 0x800, v22
	s_nop 1
	v_lshrrev_b32_e32 v250, 6, v0
	v_and_b32_e32 v251, 1, v250
	v_lshrrev_b32_e32 v250, 1, v250
	v_lshlrev_b32_e32 v250, 11, v250
	v_lshl_or_b32 v250, v251, 13, v250
	v_and_b32_e32 v251, 63, v0
	v_lshl_or_b32 v250, v251, 4, v250
	v_mov_b32_e32 v251, s22
	v_lshl_add_u32 v250, v251, 14, v250
	v_add_u32_e32 v250, 0x4b182000, v250
	v_mov_b32_e32 v251, 0
	v_lshl_add_u64 v[250:251], s[8:9], 0, v[250:251]
	global_store_dwordx4 v[250:251], v[6:9], off
	s_nop 1
	v_lshlrev_b64 v[6:7], 2, v[82:83]
	v_lshl_add_u64 v[12:13], v[16:17], 0, v[6:7]
	s_nop 0
	v_or_b32_e32 v8, 16, v11
	v_mad_u64_u32 v[10:11], s[4:5], v8, s92, v[10:11]
	v_add_u32_e32 v8, 0x4800, v10
	ds_read2_b64 v[10:13], v8 offset0:128 offset1:132
	v_or_b32_e32 v82, 0xc00, v22
	v_lshlrev_b64 v[22:23], 2, v[82:83]
	s_waitcnt lgkmcnt(0)
	v_mfma_f32_16x16x32_bf16 v[2:5], v[2:5], v[10:13], 0
	v_lshl_add_u64 v[16:17], v[16:17], 0, v[22:23]
	s_nop 0
	v_lshl_add_u64 v[8:9], v[14:15], 0, s[42:43]
	v_lshl_add_u64 v[10:11], v[8:9], 0, v[20:21]
	s_nop 3
	global_store_dwordx4 v[250:251], v[2:5], off offset:1024
	s_nop 1
	v_lshl_add_u64 v[2:3], v[8:9], 0, v[6:7]
	s_nop 0
	v_lshl_add_u64 v[2:3], v[8:9], 0, v[22:23]
	s_nop 0
	s_mov_b64 s[4:5], 0

; __device__ __forceinline__ void hgrn_x2_unit(const Args& a, int unit) {
;     ...
;     const int vs = unit & 7, h = (unit >> 3) & 7, b = unit >> 6;
;     const bf16* QT = (const bf16*)(ws + WS_HQT); float* OI = (float*)(ws + WS_HOI);
;     const int fr = lane & 15, fg = lane >> 4;
;     f32x4 S[8];
; #pragma unroll
;     for (int i = 0; i < 8; ++i) S[i] = (f32x4){0.f, 0.f, 0.f, 0.f};
; #pragma unroll 1
;     for (int blk = 0; blk < SEQ / HB; ++blk) {
;         const int u = (b * 8 + h) * 64 + blk; const size_t tok0 = (size_t)b * SEQ + blk * HB;
;         const bf16* KT = (const bf16*)(ws + WS_HKT) + (size_t)u * 4096; const bf16* VT = (const bf16*)(ws + WS_HVT) + (size_t)u * 4096; const float* DEC = (const float*)(ws + WS_HDEC) + (size_t)u * 128;
;         FragU Aq[2][4]; f32x4 o[2]; FragU Ak[8]; f32x4 dc[8]; FragU Bv;
; #pragma unroll
;         for (int mt = 0; mt < 2; ++mt) { const bf16* qr = QT + (tok0 + 16 * mt + fr) * 1024 + h * 128;
; #pragma unroll
;             for (int ks = 0; ks < 4; ++ks) { Aq[mt][ks].h[0] = *(const u32x2*)(qr + 32 * ks + 4 * fg); Aq[mt][ks].h[1] = *(const u32x2*)(qr + 32 * ks + 16 + 4 * fg); }
; #pragma unroll
;             for (int r = 0; r < 4; ++r) o[mt][r] = OI[(tok0 + 16 * mt + 4 * fg + r) * 1024 + h * 128 + 16 * vs + fr]; }
; #pragma unroll
;         for (int dt = 0; dt < 8; ++dt) { Ak[dt].u = *(const u32x4*)(KT + (16 * dt + fr) * 32 + 8 * fg); dc[dt] = *(const f32x4*)(DEC + 16 * dt + 4 * fg); }
;         Bv.u = *(const u32x4*)(VT + (16 * vs + fr) * 32 + 8 * fg);
.LBB0_733:
	s_andn2_b64 vcc, exec, s[6:7]
	s_cbranch_vccnz .LBB0_736
	s_lshl_b32 s4, s60, 1
	s_add_i32 s14, s2, s4
	v_mov_b32_e32 v1, v0
	s_mov_b64 s[4:5], 0
	s_ashr_i32 s8, s14, 6
	s_load_dwordx2 s[6:7], s[0:1], 0xd0
	s_ashr_i32 s9, s8, 31
	v_and_b32_e32 v4, 15, v1
	v_bfe_u32 v1, v1, 4, 2
	s_lshl_b64 s[10:11], s[8:9], 23
	s_bfe_u32 s15, s14, 0x30003
	v_lshl_or_b32 v2, v1, 14, s10
	s_and_b32 s14, s14, 7
	v_lshl_or_b32 v2, s15, 9, v2
	s_lshl_b32 s10, s14, 6
	v_lshlrev_b32_e32 v3, 2, v4
	s_lshl_b32 s16, s8, 9
	v_or3_b32 v2, v2, s10, v3
	v_mov_b32_e32 v3, s11
	s_lshl_b64 s[8:9], s[8:9], 22
	s_lshl_b32 s17, s15, 6
	v_lshlrev_b32_e32 v5, 3, v1
	s_waitcnt vmcnt(8) lgkmcnt(0)
	v_lshl_add_u64 v[46:47], s[6:7], 0, v[2:3]
	v_lshl_or_b32 v2, v4, 11, s8
	s_lshl_b32 s8, s15, 8
	v_or3_b32 v2, v2, s8, v5
	s_or_b32 s8, s16, s17
	v_mov_b32_e32 v3, s9
	s_ashr_i32 s9, s8, 31
	v_and_b32_e32 v250, 63, v0
	v_lshlrev_b32_e32 v250, 4, v250
	s_mul_i32 vcc_lo, s8, 0x2000
	v_add_u32_e32 v250, vcc_lo, v250
	v_mov_b32_e32 v251, 0
	v_lshl_add_u64 v[48:49], s[6:7], 0, v[250:251]
	v_and_b32_e32 v170, 63, v0
	v_lshlrev_b32_e32 v170, 4, v170
	s_mul_i32 vcc_lo, s8, 0x4000
	v_add_u32_e32 v170, vcc_lo, v170
	s_mul_i32 vcc_lo, s14, 0x400
	v_add_u32_e32 v170, vcc_lo, v170
	v_add_u32_e32 v170, 0x4b182000, v170
	v_add_u32_e32 v172, 0x2000, v170
	v_mov_b32_e32 v171, 0
	v_mov_b32_e32 v173, 0
	v_lshl_add_u64 v[170:171], s[6:7], 0, v[170:171]
	v_lshl_add_u64 v[172:173], s[6:7], 0, v[172:173]
	s_lshl_b64 s[10:11], s[8:9], 13
	v_lshlrev_b32_e32 v2, 4, v1
	v_or_b32_e32 v1, s10, v2
	s_lshl_b32 s10, s14, 10
	v_lshlrev_b32_e32 v8, 6, v4
	v_or3_b32 v4, s10, v8, v1
	v_mov_b32_e32 v5, s11
	v_lshl_add_u64 v[6:7], s[6:7], 0, v[4:5]
	v_or_b32_e32 v4, v1, v8
	s_lshl_b64 s[8:9], s[8:9], 9
	v_lshl_add_u64 v[52:53], s[6:7], 0, v[4:5]
	s_add_u32 s6, s6, s8
	v_mov_b32_e32 v3, 0
	s_addc_u32 s7, s7, s9
	s_mov_b64 s[10:11], 0x47c82000
	v_lshl_add_u64 v[4:5], s[6:7], 0, v[2:3]
	s_mov_b64 s[6:7], 0x48c82100
	v_lshl_add_u64 v[50:51], v[6:7], 0, s[10:11]
	v_lshl_add_u64 v[54:55], v[4:5], 0, s[6:7]
	s_mov_b32 s16, 64
	s_mov_b32 s17, 0x45c82000
	s_mov_b32 s18, 0x48d83000
	s_mov_b32 s19, 0x48d85000
	s_mov_b32 s20, 0x45c83000
	s_mov_b32 s21, 0x48d93000
	s_mov_b32 s22, 0x48d95000
	s_mov_b32 s23, 0x46c82000
	s_mov_b32 s24, 0x46c83000
	s_mov_b64 s[6:7], 0x20000
	s_mov_b64 s[8:9], 0x2000
	s_mov_b64 s[10:11], 0x2000
	s_mov_b64 s[14:15], 0x200
	v_mov_b32_e32 v2, v3
	v_mov_b32_e32 v4, v3
	v_mov_b32_e32 v5, v3
	v_mov_b32_e32 v6, v3
	v_mov_b32_e32 v7, v3
	v_mov_b32_e32 v8, v3
	v_mov_b32_e32 v9, v3
	v_mov_b32_e32 v10, v3
	v_mov_b32_e32 v11, v3
	v_mov_b32_e32 v12, v3
	v_mov_b32_e32 v13, v3
	v_mov_b32_e32 v14, v3
	v_mov_b32_e32 v15, v3
	v_mov_b32_e32 v16, v3
	v_mov_b32_e32 v17, v3
	v_mov_b32_e32 v18, v3
	v_mov_b32_e32 v19, v3
	v_mov_b32_e32 v20, v3
	v_mov_b32_e32 v21, v3
	v_mov_b32_e32 v22, v3
	v_mov_b32_e32 v23, v3
	v_mov_b32_e32 v24, v3
	v_mov_b32_e32 v25, v3
	v_mov_b32_e32 v26, v3
	v_mov_b32_e32 v27, v3
	v_mov_b32_e32 v28, v3
	v_mov_b32_e32 v29, v3
	v_mov_b32_e32 v30, v3
	v_mov_b32_e32 v31, v3
	v_mov_b32_e32 v32, v3
	v_mov_b32_e32 v33, v3
; __device__ __forceinline__ unsigned pk2(float lo, float hi) { unsigned r; asm volatile("v_cvt_pk_bf16_f32 %0, %1, %2" : "=v"(r) : "v"(lo), "v"(hi)); return r; }
; __device__ __forceinline__ f32x4 mfma16(bf16x8 a, bf16x8 b, f32x4 c) { return __builtin_amdgcn_mfma_f32_16x16x32_bf16(a, b, c, 0, 0, 0); }
; __device__ __forceinline__ void hgrn_x2_unit(const Args& a, int unit) {
;     ...
;     for (int blk = 0; blk < SEQ / HB; ++blk) {
;         const int u = (b * 8 + h) * 64 + blk; const size_t tok0 = (size_t)b * SEQ + blk * HB;
;         const bf16* KT = (const bf16*)(ws + WS_HKT) + (size_t)u * 4096; const bf16* VT = (const bf16*)(ws + WS_HVT) + (size_t)u * 4096; const float* DEC = (const float*)(ws + WS_HDEC) + (size_t)u * 128;
;         FragU Aq[2][4]; f32x4 o[2]; FragU Ak[8]; f32x4 dc[8]; FragU Bv;
; #pragma unroll
;         for (int mt = 0; mt < 2; ++mt) { const bf16* qr = QT + (tok0 + 16 * mt + fr) * 1024 + h * 128;
; #pragma unroll
;             for (int ks = 0; ks < 4; ++ks) { Aq[mt][ks].h[0] = *(const u32x2*)(qr + 32 * ks + 4 * fg); Aq[mt][ks].h[1] = *(const u32x2*)(qr + 32 * ks + 16 + 4 * fg); }
; #pragma unroll
;             for (int r = 0; r < 4; ++r) o[mt][r] = OI[(tok0 + 16 * mt + 4 * fg + r) * 1024 + h * 128 + 16 * vs + fr]; }
; #pragma unroll
;         for (int dt = 0; dt < 8; ++dt) { Ak[dt].u = *(const u32x4*)(KT + (16 * dt + fr) * 32 + 8 * fg); dc[dt] = *(const f32x4*)(DEC + 16 * dt + 4 * fg); }
;         Bv.u = *(const u32x4*)(VT + (16 * vs + fr) * 32 + 8 * fg);
; #pragma unroll
;         for (int ks = 0; ks < 4; ++ks) { FragU Sb; Sb.u.x = pk2(S[2 * ks][0], S[2 * ks][1]); Sb.u.y = pk2(S[2 * ks][2], S[2 * ks][3]); Sb.u.z = pk2(S[2 * ks + 1][0], S[2 * ks + 1][1]); Sb.u.w = pk2(S[2 * ks + 1][2], S[2 * ks + 1][3]);
;             o[0] = mfma16(Aq[0][ks].v, Sb.v, o[0]); o[1] = mfma16(Aq[1][ks].v, Sb.v, o[1]); }
; #pragma unroll
;         for (int mt = 0; mt < 2; ++mt)
; #pragma unroll
;             for (int r = 0; r < 4; ++r) OI[(tok0 + 16 * mt + 4 * fg + r) * 1024 + h * 128 + 16 * vs + fr] = o[mt][r];
; #pragma unroll
;         for (int dt = 0; dt < 8; ++dt) S[dt] = mfma16(Ak[dt].v, Bv.v, S[dt] * dc[dt]);
.LBB0_735:
	v_lshl_add_u64 v[34:35], v[48:49], 0, s[4:5]
	v_add_co_u32_e32 v120, vcc, s17, v34
	v_lshl_add_u64 v[36:37], v[46:47], 0, s[4:5]
	s_nop 0
	v_addc_co_u32_e32 v121, vcc, 0, v35, vcc
	v_add_co_u32_e32 v56, vcc, s18, v36
	v_lshl_add_u64 v[40:41], v[52:53], 0, s[4:5]
	s_nop 0
	v_addc_co_u32_e32 v57, vcc, 0, v37, vcc
	v_add_co_u32_e32 v58, vcc, s19, v36
	v_lshl_add_u64 v[38:39], v[54:55], 0, s[4:5]
	s_nop 0
	v_addc_co_u32_e32 v59, vcc, 0, v37, vcc
	v_add_co_u32_e32 v122, vcc, s20, v34
	v_lshl_add_u64 v[156:157], v[50:51], 0, s[4:5]
	s_nop 0
	v_addc_co_u32_e32 v123, vcc, 0, v35, vcc
	v_add_co_u32_e32 v60, vcc, s21, v36
	s_add_i32 s16, s16, -1
	s_nop 0
	v_addc_co_u32_e32 v61, vcc, 0, v37, vcc
	v_add_co_u32_e32 v62, vcc, s22, v36
	v_lshl_add_u64 v[46:47], v[46:47], 0, s[6:7]
	s_nop 0
	v_addc_co_u32_e32 v63, vcc, 0, v37, vcc
	v_add_co_u32_e32 v132, vcc, s23, v40
	v_lshl_add_u64 v[48:49], v[48:49], 0, s[8:9]
	s_nop 0
	v_addc_co_u32_e32 v133, vcc, 0, v41, vcc
	v_add_co_u32_e32 v152, vcc, s24, v40
	v_lshl_add_u64 v[50:51], v[50:51], 0, s[10:11]
	s_nop 0
	v_addc_co_u32_e32 v153, vcc, 0, v41, vcc
	global_load_dwordx4 v[64:67], v[38:39], off offset:-256
	global_load_dwordx4 v[68:71], v[38:39], off offset:-192
	global_load_dwordx4 v[72:75], v[38:39], off offset:-128
	global_load_dwordx4 v[76:79], v[38:39], off offset:-64
	global_load_dwordx4 v[80:83], v[38:39], off
	global_load_dwordx4 v[84:87], v[38:39], off offset:64
	global_load_dwordx4 v[88:91], v[38:39], off offset:128
	global_load_dwordx4 v[92:95], v[38:39], off offset:192
	global_load_dwordx4 v[96:99], v[120:121], off
	s_nop 0
	global_load_dwordx4 v[100:103], v[120:121], off offset:1024
	s_nop 0
	global_load_dwordx4 v[104:107], v[120:121], off offset:2048
	s_nop 0
	global_load_dwordx4 v[34:37], v[120:121], off offset:3072
	s_nop 0
	global_load_dwordx4 v[108:111], v[122:123], off
	s_nop 0
	global_load_dwordx4 v[112:115], v[122:123], off offset:1024
	s_nop 0
	global_load_dwordx4 v[42:45], v[122:123], off offset:2048
	s_nop 0
	global_load_dwordx4 v[38:41], v[122:123], off offset:3072
	s_nop 0
	global_load_dwordx4 v[116:119], v[170:171], off
	s_nop 0
	s_nop 0
	s_nop 0
	global_load_dwordx4 v[120:123], v[172:173], off
	s_nop 0
	s_nop 0
	s_nop 0
	global_load_dwordx4 v[124:127], v[132:133], off offset:1024
	global_load_dwordx4 v[128:131], v[132:133], off offset:2048
	s_nop 0
	global_load_dwordx4 v[132:135], v[132:133], off offset:3072
	s_nop 0
	global_load_dwordx4 v[136:139], v[152:153], off offset:-4096
	global_load_dwordx4 v[140:143], v[152:153], off
	global_load_dwordx4 v[144:147], v[152:153], off offset:1024
	global_load_dwordx4 v[148:151], v[152:153], off offset:2048
	s_nop 0
	global_load_dwordx4 v[152:155], v[152:153], off offset:3072
	s_nop 0
	global_load_dwordx4 v[156:159], v[156:157], off
	v_lshl_add_u64 v[170:171], v[170:171], 0, s[10:11]
	v_lshl_add_u64 v[170:171], v[170:171], 0, s[10:11]
	v_lshl_add_u64 v[172:173], v[172:173], 0, s[10:11]
	v_lshl_add_u64 v[172:173], v[172:173], 0, s[10:11]
	v_cvt_pk_bf16_f32 v160, v2, v3
	v_cvt_pk_bf16_f32 v161, v4, v5
	v_cvt_pk_bf16_f32 v162, v6, v7
	v_cvt_pk_bf16_f32 v163, v8, v9
	v_cvt_pk_bf16_f32 v164, v10, v11
	v_cvt_pk_bf16_f32 v165, v12, v13
	v_cvt_pk_bf16_f32 v166, v14, v15
	v_cvt_pk_bf16_f32 v167, v16, v17
	v_lshl_add_u64 v[52:53], v[52:53], 0, s[10:11]
	v_lshl_add_u64 v[54:55], v[54:55], 0, s[14:15]
	s_cmp_eq_u32 s16, 0
	s_waitcnt vmcnt(10)
	v_mfma_f32_16x16x32_bf16 v[96:99], v[96:99], v[160:163], v[116:119]
	v_mul_f32_e64 v6, v6, v68
	v_mul_f32_e64 v7, v7, v69
	v_pk_mul_f32 v[8:9], v[8:9], v[70:71]
	v_cvt_pk_bf16_f32 v116, v18, v19
	s_waitcnt vmcnt(9)
	v_mfma_f32_16x16x32_bf16 v[108:111], v[108:111], v[160:163], v[120:123]
	v_cvt_pk_bf16_f32 v117, v20, v21
	v_cvt_pk_bf16_f32 v118, v22, v23
	v_mul_f32_e64 v10, v10, v72
	v_mul_f32_e64 v11, v11, v73
	v_mfma_f32_16x16x32_bf16 v[68:71], v[100:103], v[164:167], v[96:99]
	v_mul_f32_e64 v12, v12, v74
	v_mul_f32_e64 v13, v13, v75
	v_cvt_pk_bf16_f32 v119, v24, v25
	v_pk_mul_f32 v[2:3], v[2:3], v[64:65]
	v_mfma_f32_16x16x32_bf16 v[72:75], v[112:115], v[164:167], v[108:111]
	v_mul_f32_e64 v4, v4, v66
	v_mul_f32_e64 v5, v5, v67
	v_pk_mul_f32 v[14:15], v[14:15], v[76:77]
	v_pk_mul_f32 v[16:17], v[16:17], v[78:79]
	v_mfma_f32_16x16x32_bf16 v[68:71], v[104:107], v[116:119], v[68:71]
	v_cvt_pk_bf16_f32 v64, v26, v27
	v_mul_f32_e64 v18, v18, v80
	v_mul_f32_e64 v19, v19, v81
	v_pk_mul_f32 v[20:21], v[20:21], v[82:83]
	v_cvt_pk_bf16_f32 v65, v28, v29
	v_pk_mul_f32 v[22:23], v[22:23], v[84:85]
	v_pk_mul_f32 v[24:25], v[24:25], v[86:87]
	v_cvt_pk_bf16_f32 v66, v30, v31
	v_pk_mul_f32 v[26:27], v[26:27], v[88:89]
	v_pk_mul_f32 v[28:29], v[28:29], v[90:91]
	v_cvt_pk_bf16_f32 v67, v32, v33
	v_pk_mul_f32 v[30:31], v[30:31], v[92:93]
	v_pk_mul_f32 v[32:33], v[32:33], v[94:95]
	s_waitcnt vmcnt(0)
	v_mfma_f32_16x16x32_bf16 v[2:5], v[136:139], v[156:159], v[2:5]
	v_mfma_f32_16x16x32_bf16 v[6:9], v[124:127], v[156:159], v[6:9]
	v_mfma_f32_16x16x32_bf16 v[10:13], v[128:131], v[156:159], v[10:13]
	v_mfma_f32_16x16x32_bf16 v[14:17], v[132:135], v[156:159], v[14:17]
	v_mfma_f32_16x16x32_bf16 v[18:21], v[140:143], v[156:159], v[18:21]
	v_mfma_f32_16x16x32_bf16 v[22:25], v[144:147], v[156:159], v[22:25]
	v_mfma_f32_16x16x32_bf16 v[26:29], v[148:151], v[156:159], v[26:29]
	v_mfma_f32_16x16x32_bf16 v[30:33], v[152:155], v[156:159], v[30:33]
	v_mfma_f32_16x16x32_bf16 v[42:45], v[42:45], v[116:119], v[72:75]
	v_mfma_f32_16x16x32_bf16 v[34:37], v[34:37], v[64:67], v[68:71]
	v_mfma_f32_16x16x32_bf16 v[38:41], v[38:41], v[64:67], v[42:45]
	s_nop 6
	global_store_dword v[56:57], v34, off offset:-4096
	global_store_dword v[56:57], v35, off
	global_store_dword v[58:59], v36, off offset:-4096
	global_store_dword v[58:59], v37, off
	global_store_dword v[60:61], v38, off offset:-4096
	global_store_dword v[60:61], v39, off
	global_store_dword v[62:63], v40, off offset:-4096
	global_store_dword v[62:63], v41, off
	s_cbranch_scc0 .LBB0_735

; #define LAS __attribute__((address_space(3)))
; __device__ __forceinline__ float bf2f(bf16 b) { return __uint_as_float(((unsigned)b) << 16); }
; __device__ __forceinline__ void hgrn_x1_unit(const Args& a, int layer, int unit, LAS unsigned char* lds) {
;     int tid = threadIdx.x; asm volatile("" : "+v"(tid)); const int lane = tid & 63; const int wave = __builtin_amdgcn_readfirstlane(tid >> 6);
;     size_t wz_ = 0; asm volatile("" : "+s"(wz_)); unsigned char* ws = a.ws + wz_;
;     const int blk = unit & 63, h = (unit >> 6) & 7, b = unit >> 9;
;     const bf16* PROJ = (const bf16*)(ws + WS_PROJ);
;     bf16* QT = (bf16*)(ws + WS_HQT); bf16* KT = (bf16*)(ws + WS_HKT) + (size_t)unit * 4096; bf16* VT = (bf16*)(ws + WS_HVT) + (size_t)unit * 4096;
;     float* DEC = (float*)(ws + WS_HDEC) + (size_t)unit * 128; float* OI = (float*)(ws + WS_HOI);
;     LAS float* TOT = (LAS float*)(lds + HX_TOT);
;     const size_t tok0 = (size_t)b * SEQ + blk * HB;
;     const int d = tid & 127, tq = tid >> 7;
;     const float lb = ((const float*)(ws + WS_LB))[layer * 1024 + h * 128 + d];
;     float q[8], kk[8], c[8]; unsigned short vv[8];
;     float run = 0.f;
; #pragma unroll
;     for (int i = 0; i < 8; ++i) {
;         const bf16* pr = PROJ + (tok0 + 8 * tq + i) * DIN + h * 128 + d;
;         q[i] = bf2f(pr[C_QA]); vv[i] = pr[C_IA];
;         float z = bf2f(pr[C_FA]); z = fminf(fmaxf(z, -30.f), 30.f);
;         const float e = __expf(-z), sp = 1.0f / (1.0f + e), sn = e / (1.0f + e);
;         const float f = lb + (1.0f - lb) * sp; kk[i] = (1.0f - lb) * sn;
;         run += __logf(f); c[i] = run;
; template <int LAYER>
; __device__ __forceinline__ void layer_phases(const Args& args, LAS unsigned char* lds, const XcdBarrier& bar, int lo, int hi) {
;     ...
;             if (threadIdx.x == 0) *slot = (int)__hip_atomic_fetch_add(ctr, 1u, __ATOMIC_RELAXED, __HIP_MEMORY_SCOPE_AGENT);
;             __syncthreads();
;             const int it = __builtin_amdgcn_readfirstlane(*slot);
;             if (it >= 256 + 1024 + 2048) break;
;             if (it < 256) s5_unit(args, LAYER, it, lds);
;             else if (it < 1280) { const int j = it - 256, n = 31 - (j >> 5), b = (j >> 3) & 3, hp = j & 7, n0_ = (b & 1) ? 31 - n : n; attn_item(args, LAYER, b * 256 + n0_ * 8 + hp, lds); }
;             else hgrn_x1_unit(args, LAYER, it - 1280, lds);
.LBB0_1388:
	s_or_b64 exec, exec, s[4:5]
	s_waitcnt lgkmcnt(0)
	s_barrier
	ds_read_b32 v2, v1
	s_mov_b64 s[4:5], -1
	s_waitcnt lgkmcnt(0)
	v_readfirstlane_b32 s2, v2
	s_cmpk_gt_i32 s2, 0xcff
	s_cbranch_scc1 .LBB0_1383
	s_cmpk_gt_i32 s2, 0xff
	s_cbranch_scc0 .LBB0_1416
	s_cmpk_gt_u32 s2, 0x4ff
	s_cbranch_scc0 .LBB0_1394
	s_add_i32 s12, s2, 0xfffffb00
	v_mov_b32_e32 v14, v0
	s_mov_b64 s[4:5], 0
	s_add_u32 s42, s10, s4
	s_addc_u32 s43, s11, s5
	s_lshl_b32 s4, s12, 2
	s_lshl_b32 s5, s12, 5
	s_and_b32 s4, s4, 0x1800
	s_and_b32 s5, s5, 0x7e0
	s_or_b32 s46, s4, s5
	s_lshl_b32 s4, s12, 1
	v_and_b32_e32 v15, 0x7f, v14
	s_and_b32 s48, s4, 0x380
	v_or_b32_e32 v2, s48, v15
	v_lshlrev_b32_e32 v82, 2, v2
	v_lshl_add_u64 v[2:3], s[42:43], 0, v[82:83]
	s_mov_b32 s4, 0x21481000
	v_add_co_u32_e32 v10, vcc, s4, v2
	s_lshl_b32 s4, s48, 1
	v_ashrrev_i32_e32 v16, 7, v14
	s_add_u32 s4, s42, s4
	v_lshlrev_b32_e32 v2, 3, v16
	v_lshlrev_b32_e32 v82, 1, v15
	s_addc_u32 s5, s43, 0
	s_mov_b32 s47, s13
	v_addc_co_u32_e32 v11, vcc, 0, v3, vcc
	v_ashrrev_i32_e32 v3, 31, v2
	v_lshl_add_u64 v[6:7], s[4:5], 0, v[82:83]
	s_mov_b64 s[4:5], 0x2d482000
	v_lshl_add_u64 v[4:5], v[2:3], 0, s[46:47]
	v_lshl_add_u64 v[8:9], v[6:7], 0, s[4:5]
	v_mad_i64_i32 v[8:9], s[4:5], v4, s60, v[8:9]
	s_movk_i32 s5, 0x6000
	s_nop 0
	v_add_co_u32_e32 v12, vcc, s5, v8
	s_movk_i32 s4, 0x5000
	s_nop 0
	v_addc_co_u32_e32 v13, vcc, 0, v9, vcc
	global_load_dword v23, v[10:11], off
	global_load_ushort v20, v[12:13], off
	global_load_ushort v21, v[8:9], off offset:2048
	v_add_co_u32_e32 v10, vcc, s4, v8
	s_movk_i32 s4, 0x1000
	s_nop 0
	v_addc_co_u32_e32 v11, vcc, 0, v9, vcc
	s_waitcnt vmcnt(18)
	v_add_co_u32_e32 v18, vcc, s4, v8
	s_mov_b32 s4, 0xb000
	s_nop 0
	v_addc_co_u32_e32 v19, vcc, 0, v9, vcc
	global_load_ushort v17, v[12:13], off offset:2048
	s_nop 0
	global_load_ushort v18, v[18:19], off
	s_nop 0
	global_load_ushort v12, v[8:9], off
	global_load_ushort v13, v[10:11], off offset:2048
	v_add_co_u32_e32 v10, vcc, s4, v8
	v_lshl_add_u64 v[6:7], v[6:7], 0, s[20:21]
	s_nop 0
	v_addc_co_u32_e32 v11, vcc, 0, v9, vcc
	global_load_ushort v36, v[10:11], off offset:2048
	v_lshlrev_b64 v[4:5], 11, v[4:5]
	v_readfirstlane_b32 s49, v14
	s_waitcnt vmcnt(7)
	v_sub_f32_e32 v24, 1.0, v23
	s_waitcnt vmcnt(6)
	v_lshlrev_b32_e32 v11, 16, v20
	s_waitcnt vmcnt(5)
	v_lshlrev_b32_e32 v10, 16, v21
	v_max_f32_e32 v10, v10, v10
	v_med3_f32 v10, v10, s61, v102
	v_mul_f32_e32 v10, 0xbfb8aa3b, v10
	v_exp_f32_e32 v10, v10
	v_max_f32_e32 v11, v11, v11
	v_med3_f32 v11, v11, s61, v102
	v_mul_f32_e32 v11, 0xbfb8aa3b, v11
	v_exp_f32_e32 v37, v11
	v_add_f32_e32 v11, 1.0, v10
	s_waitcnt vmcnt(2)
	v_lshlrev_b32_e32 v20, 16, v12
	v_div_scale_f32 v12, s[4:5], v11, v11, 1.0
	v_rcp_f32_e32 v26, v12
	v_div_scale_f32 v21, s[4:5], v11, v11, v10
	v_rcp_f32_e32 v27, v21
	v_fma_f32 v30, -v12, v26, 1.0
	s_waitcnt vmcnt(1)
	v_lshlrev_b32_e32 v19, 16, v13
	v_div_scale_f32 v13, vcc, 1.0, v11, 1.0
	v_fmac_f32_e32 v26, v30, v26
	v_mul_f32_e32 v30, v13, v26
	v_fma_f32 v31, -v21, v27, 1.0
	v_fma_f32 v33, -v12, v30, v13
	v_div_scale_f32 v22, s[4:5], v10, v11, v10
	v_fmac_f32_e32 v27, v31, v27
	v_fmac_f32_e32 v30, v33, v26
	v_mul_f32_e32 v31, v22, v27
	v_fma_f32 v12, -v12, v30, v13
	v_fma_f32 v34, -v21, v31, v22
	v_div_fmas_f32 v12, v12, v26, v30
	v_fmac_f32_e32 v31, v34, v27
	v_div_fixup_f32 v12, v12, v11, 1.0
	v_fma_f32 v13, -v21, v31, v22
	s_mov_b64 vcc, s[4:5]
	v_fma_f32 v12, v24, v12, v23
	v_div_fmas_f32 v13, v13, v27, v31
	v_cmp_gt_f32_e32 vcc, s62, v12
	v_add_f32_e32 v38, 1.0, v37
	v_div_scale_f32 v25, s[6:7], v38, v38, 1.0
	v_cndmask_b32_e64 v21, 0, 32, vcc
	v_ldexp_f32 v12, v12, v21
	v_log_f32_e32 v12, v12
	v_rcp_f32_e32 v28, v25
	v_div_fixup_f32 v10, v13, v11, v10
	v_div_scale_f32 v29, s[6:7], 1.0, v38, 1.0
	v_mul_f32_e32 v11, 0x3f317217, v12
	v_fma_f32 v11, v12, s63, -v11
	v_fma_f32 v32, -v25, v28, 1.0
	v_fmac_f32_e32 v11, 0x3377d1cf, v12
	v_fmac_f32_e32 v28, v32, v28
	v_mul_f32_e32 v21, v24, v10
	v_cndmask_b32_e32 v10, 0, v103, vcc
	v_fmac_f32_e32 v11, 0x3f317217, v12
	v_cmp_lt_f32_e64 vcc, |v12|, s64
	v_mul_f32_e32 v32, v29, v28
	v_fma_f32 v35, -v25, v32, v29
	v_cndmask_b32_e32 v11, v12, v11, vcc
	v_div_scale_f32 v12, s[4:5], v38, v38, v37
	v_rcp_f32_e32 v39, v12
	v_fmac_f32_e32 v32, v35, v28
	v_sub_f32_e32 v10, v11, v10
	v_add_f32_e32 v22, 0, v10
	v_fma_f32 v10, -v25, v32, v29
	s_mov_b64 vcc, s[6:7]
	v_div_fmas_f32 v10, v10, v28, v32
	v_div_fixup_f32 v13, v10, v38, 1.0
	v_fma_f32 v10, -v12, v39, 1.0
	v_fmac_f32_e32 v39, v10, v39
	v_div_scale_f32 v25, vcc, v37, v38, v37
	s_mov_b32 s4, 0xc000
	v_mul_f32_e32 v40, v25, v39
	v_add_co_u32_e64 v10, s[4:5], s4, v8
	v_fma_f32 v26, -v12, v40, v25
	s_nop 0
	v_addc_co_u32_e64 v11, s[4:5], 0, v9, s[4:5]
	v_fmac_f32_e32 v40, v26, v39
	s_mov_b32 s4, 0x10000
	global_load_ushort v41, v[10:11], off offset:-4096
	v_fma_f32 v42, -v12, v40, v25
	v_add_co_u32_e64 v12, s[4:5], s4, v8
	v_fma_f32 v43, v24, v13, v23
	s_nop 0
	v_addc_co_u32_e64 v13, s[4:5], 0, v9, s[4:5]
	s_mov_b32 s4, 0x11000
	s_nop 0
	v_add_co_u32_e64 v28, s[4:5], s4, v8
	s_waitcnt vmcnt(0)
; __device__ __forceinline__ float bf2f(bf16 b) { return __uint_as_float(((unsigned)b) << 16); }
; __device__ __forceinline__ void hgrn_x1_unit(const Args& a, int layer, int unit, LAS unsigned char* lds) {
;     ...
;     for (int i = 0; i < 8; ++i) {
;         const bf16* pr = PROJ + (tok0 + 8 * tq + i) * DIN + h * 128 + d;
;         q[i] = bf2f(pr[C_QA]); vv[i] = pr[C_IA];
;         float z = bf2f(pr[C_FA]); z = fminf(fmaxf(z, -30.f), 30.f);
;         const float e = __expf(-z), sp = 1.0f / (1.0f + e), sn = e / (1.0f + e);
;         const float f = lb + (1.0f - lb) * sp; kk[i] = (1.0f - lb) * sn;
;         run += __logf(f); c[i] = run;
;     }
	v_lshlrev_b32_e32 v54, 16, v41
	v_addc_co_u32_e64 v29, s[4:5], 0, v9, s[4:5]
	s_mov_b32 s4, 0x16000
	s_nop 0
	v_add_co_u32_e64 v26, s[4:5], s4, v8
	s_nop 1
	v_addc_co_u32_e64 v27, s[4:5], 0, v9, s[4:5]
	v_add_co_u32_e64 v30, s[4:5], s67, v8
	s_nop 1
	v_addc_co_u32_e64 v31, s[4:5], 0, v9, s[4:5]
	v_add_co_u32_e64 v32, s[4:5], s68, v8
	s_nop 1
	v_addc_co_u32_e64 v33, s[4:5], 0, v9, s[4:5]
	v_add_co_u32_e64 v34, s[4:5], s69, v8
	s_nop 1
	v_addc_co_u32_e64 v35, s[4:5], 0, v9, s[4:5]
	global_load_ushort v44, v[12:13], off offset:2048
	global_load_ushort v25, v[28:29], off offset:2048
	global_load_ushort v45, v[26:27], off offset:2048
	global_load_ushort v46, v[30:31], off offset:2048
	s_nop 0
	global_load_ushort v26, v[32:33], off offset:2048
	s_nop 0
	global_load_ushort v34, v[34:35], off offset:2048
	s_nop 0
	global_load_ushort v32, v[32:33], off
	s_nop 0
	global_load_ushort v33, v[28:29], off
	v_cmp_gt_f32_e64 s[4:5], s62, v43
	v_div_fmas_f32 v13, v42, v39, v40
	v_div_fixup_f32 v13, v13, v38, v37
	v_cndmask_b32_e64 v12, 0, 32, s[4:5]
	v_ldexp_f32 v12, v43, v12
	v_log_f32_e32 v12, v12
	v_mul_f32_e32 v52, v24, v13
	v_mul_f32_e32 v13, 0x3f317217, v12
	v_fma_f32 v13, v12, s63, -v13
	v_fmac_f32_e32 v13, 0x3377d1cf, v12
	v_fmac_f32_e32 v13, 0x3f317217, v12
	v_cmp_lt_f32_e64 vcc, |v12|, s64
	s_waitcnt vmcnt(7)
	v_lshlrev_b32_e32 v57, 16, v44
	v_cndmask_b32_e32 v12, v12, v13, vcc
	v_lshlrev_b32_e32 v13, 16, v36
	v_max_f32_e32 v13, v13, v13
	v_med3_f32 v13, v13, s61, v102
	v_mul_f32_e32 v13, 0xbfb8aa3b, v13
	v_exp_f32_e32 v35, v13
	v_cndmask_b32_e64 v13, 0, v103, s[4:5]
	v_add_co_u32_e32 v28, vcc, s66, v8
	v_sub_f32_e32 v12, v12, v13
	s_nop 0
	v_addc_co_u32_e32 v29, vcc, 0, v9, vcc
	v_add_f32_e32 v53, v22, v12
	v_add_co_u32_e32 v12, vcc, s70, v8
	v_add_f32_e32 v36, 1.0, v35
	s_nop 0
	v_addc_co_u32_e32 v13, vcc, 0, v9, vcc
	v_add_co_u32_e32 v30, vcc, s72, v8
	v_div_scale_f32 v37, s[4:5], v36, v36, 1.0
	s_nop 0
	v_addc_co_u32_e32 v31, vcc, 0, v9, vcc
	global_load_ushort v10, v[10:11], off
	s_nop 0
	global_load_ushort v39, v[28:29], off offset:-4096
	global_load_ushort v11, v[28:29], off
	s_nop 0
	global_load_ushort v28, v[12:13], off offset:-4096
	global_load_ushort v27, v[30:31], off offset:2048
	v_rcp_f32_e32 v38, v37
	s_waitcnt vmcnt(5)
	v_lshlrev_b32_e32 v33, 16, v33
	v_max_f32_e32 v33, v33, v33
	v_med3_f32 v33, v33, s61, v102
	v_fma_f32 v29, -v37, v38, 1.0
	v_fmac_f32_e32 v38, v29, v38
	v_div_scale_f32 v29, vcc, 1.0, v36, 1.0
	v_mul_f32_e32 v40, v29, v38
	v_fma_f32 v41, -v37, v40, v29
	v_fmac_f32_e32 v40, v41, v38
	v_fma_f32 v29, -v37, v40, v29
	v_div_scale_f32 v37, s[4:5], v36, v36, v35
	v_rcp_f32_e32 v41, v37
	v_div_fmas_f32 v29, v29, v38, v40
	v_div_fixup_f32 v29, v29, v36, 1.0
	v_fma_f32 v29, v24, v29, v23
	v_fma_f32 v38, -v37, v41, 1.0
	v_fmac_f32_e32 v41, v38, v41
	v_div_scale_f32 v38, vcc, v35, v36, v35
	v_mul_f32_e32 v40, v38, v41
	v_fma_f32 v42, -v37, v40, v38
	v_fmac_f32_e32 v40, v42, v41
	v_cmp_gt_f32_e64 s[4:5], s62, v29
	v_fma_f32 v37, -v37, v40, v38
	v_div_fmas_f32 v37, v37, v41, v40
	v_cndmask_b32_e64 v38, 0, 32, s[4:5]
	v_ldexp_f32 v29, v29, v38
	v_log_f32_e32 v29, v29
	v_mul_f32_e32 v33, 0xbfb8aa3b, v33
	v_div_fixup_f32 v35, v37, v36, v35
	v_exp_f32_e32 v33, v33
	v_mul_f32_e32 v55, v24, v35
	v_mul_f32_e32 v35, 0x3f317217, v29
	v_fma_f32 v35, v29, s63, -v35
	v_fmac_f32_e32 v35, 0x3377d1cf, v29
	v_fmac_f32_e32 v35, 0x3f317217, v29
	v_cmp_lt_f32_e64 vcc, |v29|, s64
	v_add_f32_e32 v36, 1.0, v33
	v_lshlrev_b32_e32 v32, 16, v32
	v_cndmask_b32_e32 v29, v29, v35, vcc
	v_cndmask_b32_e64 v35, 0, v103, s[4:5]
	v_div_scale_f32 v37, s[4:5], v36, v36, 1.0
	v_rcp_f32_e32 v38, v37
	v_sub_f32_e32 v29, v29, v35
	v_add_f32_e32 v56, v53, v29
	v_max_f32_e32 v32, v32, v32
	v_fma_f32 v29, -v37, v38, 1.0
	v_fmac_f32_e32 v38, v29, v38
	v_div_scale_f32 v29, vcc, 1.0, v36, 1.0
	v_mul_f32_e32 v35, v29, v38
	v_fma_f32 v40, -v37, v35, v29
	v_fmac_f32_e32 v35, v40, v38
	v_fma_f32 v29, -v37, v35, v29
	v_div_scale_f32 v37, s[4:5], v36, v36, v33
	v_rcp_f32_e32 v40, v37
	v_div_fmas_f32 v29, v29, v38, v35
	v_div_fixup_f32 v29, v29, v36, 1.0
	v_fma_f32 v29, v24, v29, v23
	v_fma_f32 v35, -v37, v40, 1.0
	v_fmac_f32_e32 v40, v35, v40
	v_div_scale_f32 v35, vcc, v33, v36, v33
	v_mul_f32_e32 v38, v35, v40
	v_fma_f32 v41, -v37, v38, v35
	v_fmac_f32_e32 v38, v41, v40
	v_fma_f32 v35, -v37, v38, v35
	v_cmp_gt_f32_e64 s[4:5], s62, v29
	v_div_fmas_f32 v35, v35, v40, v38
	v_div_fixup_f32 v33, v35, v36, v33
	v_cndmask_b32_e64 v37, 0, 32, s[4:5]
	v_ldexp_f32 v29, v29, v37
	v_lshlrev_b32_e32 v35, 16, v45
	v_log_f32_e32 v29, v29
	v_max_f32_e32 v35, v35, v35
	v_med3_f32 v35, v35, s61, v102
	v_mul_f32_e32 v35, 0xbfb8aa3b, v35
	v_exp_f32_e32 v35, v35
	v_mul_f32_e32 v58, v24, v33
	v_mul_f32_e32 v33, 0x3f317217, v29
	v_fma_f32 v33, v29, s63, -v33
	v_fmac_f32_e32 v33, 0x3377d1cf, v29
	v_fmac_f32_e32 v33, 0x3f317217, v29
	v_cmp_lt_f32_e64 vcc, |v29|, s64
	v_add_f32_e32 v36, 1.0, v35
	s_waitcnt vmcnt(3)
; __device__ __forceinline__ float bf2f(bf16 b) { return __uint_as_float(((unsigned)b) << 16); }
; __device__ __forceinline__ void hgrn_x1_unit(const Args& a, int layer, int unit, LAS unsigned char* lds) {
;     ...
;     for (int i = 0; i < 8; ++i) {
;         const bf16* pr = PROJ + (tok0 + 8 * tq + i) * DIN + h * 128 + d;
;         q[i] = bf2f(pr[C_QA]); vv[i] = pr[C_IA];
;         float z = bf2f(pr[C_FA]); z = fminf(fmaxf(z, -30.f), 30.f);
;         const float e = __expf(-z), sp = 1.0f / (1.0f + e), sn = e / (1.0f + e);
;         const float f = lb + (1.0f - lb) * sp; kk[i] = (1.0f - lb) * sn;
;         run += __logf(f); c[i] = run;
;     }
;     __syncthreads();
;     TOT[tq * 128 + d] = run;
;     __syncthreads();
	v_lshlrev_b32_e32 v60, 16, v39
	v_cndmask_b32_e32 v29, v29, v33, vcc
	v_cndmask_b32_e64 v33, 0, v103, s[4:5]
	v_div_scale_f32 v37, s[4:5], v36, v36, 1.0
	v_rcp_f32_e32 v38, v37
	v_sub_f32_e32 v29, v29, v33
	v_add_f32_e32 v59, v56, v29
	v_med3_f32 v32, v32, s61, v102
	v_fma_f32 v29, -v37, v38, 1.0
	v_fmac_f32_e32 v38, v29, v38
	v_div_scale_f32 v29, vcc, 1.0, v36, 1.0
	v_mul_f32_e32 v33, v29, v38
	v_fma_f32 v39, -v37, v33, v29
	v_fmac_f32_e32 v33, v39, v38
	v_fma_f32 v29, -v37, v33, v29
	v_div_scale_f32 v37, s[4:5], v36, v36, v35
	v_rcp_f32_e32 v39, v37
	v_div_fmas_f32 v29, v29, v38, v33
	v_div_fixup_f32 v29, v29, v36, 1.0
	v_fma_f32 v29, v24, v29, v23
	v_fma_f32 v33, -v37, v39, 1.0
	v_fmac_f32_e32 v39, v33, v39
	v_div_scale_f32 v33, vcc, v35, v36, v35
	v_mul_f32_e32 v38, v33, v39
	v_fma_f32 v40, -v37, v38, v33
	v_fmac_f32_e32 v38, v40, v39
	v_cmp_gt_f32_e64 s[4:5], s62, v29
	v_fma_f32 v33, -v37, v38, v33
	v_div_fmas_f32 v33, v33, v39, v38
	v_cndmask_b32_e64 v37, 0, 32, s[4:5]
	v_ldexp_f32 v29, v29, v37
	v_log_f32_e32 v29, v29
	v_mul_f32_e32 v32, 0xbfb8aa3b, v32
	v_div_fixup_f32 v33, v33, v36, v35
	v_exp_f32_e32 v32, v32
	v_mul_f32_e32 v61, v24, v33
	v_mul_f32_e32 v33, 0x3f317217, v29
	v_fma_f32 v33, v29, s63, -v33
	v_fmac_f32_e32 v33, 0x3377d1cf, v29
	v_fmac_f32_e32 v33, 0x3f317217, v29
	v_cmp_lt_f32_e64 vcc, |v29|, s64
	v_add_f32_e32 v35, 1.0, v32
	s_waitcnt vmcnt(1)
	v_lshlrev_b32_e32 v66, 16, v28
	v_cndmask_b32_e32 v29, v29, v33, vcc
	v_cndmask_b32_e64 v33, 0, v103, s[4:5]
	v_div_scale_f32 v36, s[4:5], v35, v35, 1.0
	v_add_co_u32_e64 v8, s[4:5], s71, v8
	v_rcp_f32_e32 v37, v36
	s_nop 0
	v_addc_co_u32_e64 v9, s[4:5], 0, v9, s[4:5]
	global_load_ushort v8, v[8:9], off offset:2048
	s_nop 0
	global_load_ushort v9, v[30:31], off
	v_sub_f32_e32 v29, v29, v33
	v_add_f32_e32 v62, v59, v29
	v_fma_f32 v29, -v36, v37, 1.0
	v_fmac_f32_e32 v37, v29, v37
	v_div_scale_f32 v29, vcc, 1.0, v35, 1.0
	v_div_scale_f32 v30, s[4:5], v35, v35, v32
	v_mul_f32_e32 v33, v29, v37
	v_rcp_f32_e32 v31, v30
	v_fma_f32 v38, -v36, v33, v29
	v_fmac_f32_e32 v33, v38, v37
	v_fma_f32 v29, -v36, v33, v29
	v_div_fmas_f32 v29, v29, v37, v33
	v_fma_f32 v33, -v30, v31, 1.0
	v_fmac_f32_e32 v31, v33, v31
	v_div_scale_f32 v33, vcc, v32, v35, v32
	v_div_fixup_f32 v29, v29, v35, 1.0
	v_mul_f32_e32 v36, v33, v31
	v_fma_f32 v37, -v30, v36, v33
	v_fma_f32 v29, v24, v29, v23
	v_fmac_f32_e32 v36, v37, v31
	v_cmp_gt_f32_e64 s[4:5], s62, v29
	v_fma_f32 v30, -v30, v36, v33
	v_div_fmas_f32 v30, v30, v31, v36
	v_cndmask_b32_e64 v33, 0, 32, s[4:5]
	v_ldexp_f32 v29, v29, v33
	v_log_f32_e32 v29, v29
	v_lshlrev_b32_e32 v31, 16, v34
	v_max_f32_e32 v31, v31, v31
	v_div_fixup_f32 v30, v30, v35, v32
	v_med3_f32 v31, v31, s61, v102
	v_mul_f32_e32 v64, v24, v30
	v_mul_f32_e32 v30, 0x3f317217, v29
	v_mul_f32_e32 v31, 0xbfb8aa3b, v31
	v_fma_f32 v30, v29, s63, -v30
	v_exp_f32_e32 v31, v31
	v_fmac_f32_e32 v30, 0x3377d1cf, v29
	v_fmac_f32_e32 v30, 0x3f317217, v29
	v_cmp_lt_f32_e64 vcc, |v29|, s64
	global_load_ushort v67, v[12:13], off
	s_nop 0
	v_cndmask_b32_e32 v29, v29, v30, vcc
	v_cndmask_b32_e64 v30, 0, v103, s[4:5]
	v_sub_f32_e32 v29, v29, v30
	v_add_f32_e32 v30, 1.0, v31
	v_div_scale_f32 v32, s[4:5], v30, v30, 1.0
	v_rcp_f32_e32 v33, v32
	v_add_f32_e32 v65, v62, v29
	s_barrier
	v_fma_f32 v12, -v32, v33, 1.0
	v_fmac_f32_e32 v33, v12, v33
	v_div_scale_f32 v12, vcc, 1.0, v30, 1.0
	v_mul_f32_e32 v13, v12, v33
	v_fma_f32 v28, -v32, v13, v12
	v_fmac_f32_e32 v13, v28, v33
	v_div_scale_f32 v28, s[4:5], v30, v30, v31
	v_rcp_f32_e32 v29, v28
	v_fma_f32 v12, -v32, v13, v12
	v_div_fmas_f32 v12, v12, v33, v13
	v_div_fixup_f32 v12, v12, v30, 1.0
	v_fma_f32 v13, -v28, v29, 1.0
	v_fmac_f32_e32 v29, v13, v29
	v_div_scale_f32 v13, vcc, v31, v30, v31
	v_mul_f32_e32 v32, v13, v29
	v_fma_f32 v33, -v28, v32, v13
	v_fma_f32 v12, v24, v12, v23
	v_fmac_f32_e32 v32, v33, v29
	v_cmp_gt_f32_e64 s[4:5], s62, v12
	v_fma_f32 v13, -v28, v32, v13
	v_div_fmas_f32 v13, v13, v29, v32
	v_cndmask_b32_e64 v28, 0, 32, s[4:5]
	v_ldexp_f32 v12, v12, v28
	s_waitcnt vmcnt(1)
	v_lshlrev_b32_e32 v9, 16, v9
	v_log_f32_e32 v12, v12
	v_max_f32_e32 v9, v9, v9
	v_med3_f32 v9, v9, s61, v102
	v_mul_f32_e32 v9, 0xbfb8aa3b, v9
	v_div_fixup_f32 v13, v13, v30, v31
	v_exp_f32_e32 v9, v9
	v_mul_f32_e32 v68, v24, v13
	v_mul_f32_e32 v13, 0x3f317217, v12
	v_fma_f32 v13, v12, s63, -v13
	v_fmac_f32_e32 v13, 0x3377d1cf, v12
	v_fmac_f32_e32 v13, 0x3f317217, v12
	v_cmp_lt_f32_e64 vcc, |v12|, s64
	v_add_f32_e32 v28, 1.0, v9
	v_lshlrev_b32_e32 v70, 16, v8
	v_cndmask_b32_e32 v12, v12, v13, vcc
	v_cndmask_b32_e64 v13, 0, v103, s[4:5]
	v_div_scale_f32 v29, s[4:5], v28, v28, 1.0
	v_rcp_f32_e32 v30, v29
	v_sub_f32_e32 v12, v12, v13
	v_add_f32_e32 v69, v65, v12
	v_lshl_add_u64 v[36:37], v[6:7], 0, v[4:5]
	v_fma_f32 v8, -v29, v30, 1.0
	v_fmac_f32_e32 v30, v8, v30
	v_div_scale_f32 v8, vcc, 1.0, v28, 1.0
	v_mul_f32_e32 v12, v8, v30
	v_fma_f32 v13, -v29, v12, v8
	v_fmac_f32_e32 v12, v13, v30
	v_div_scale_f32 v13, s[4:5], v28, v28, v9
	v_fma_f32 v8, -v29, v12, v8
	v_rcp_f32_e32 v29, v13
	v_div_fmas_f32 v8, v8, v30, v12
	v_div_fixup_f32 v8, v8, v28, 1.0
	v_fmac_f32_e32 v23, v24, v8
	v_fma_f32 v12, -v13, v29, 1.0
	v_cmp_gt_f32_e64 s[4:5], s62, v23
	v_fmac_f32_e32 v29, v12, v29
	v_div_scale_f32 v12, vcc, v9, v28, v9
	v_cndmask_b32_e64 v8, 0, 32, s[4:5]
	v_mul_f32_e32 v30, v12, v29
	v_ldexp_f32 v8, v23, v8
	v_fma_f32 v31, -v13, v30, v12
	v_log_f32_e32 v8, v8
	v_fmac_f32_e32 v30, v31, v29
	v_fma_f32 v12, -v13, v30, v12
	v_div_fmas_f32 v12, v12, v29, v30
	v_div_fixup_f32 v23, v12, v28, v9
	v_mul_f32_e32 v9, 0x3f317217, v8
	v_fma_f32 v9, v8, s63, -v9
	v_fmac_f32_e32 v9, 0x3377d1cf, v8
	v_fmac_f32_e32 v9, 0x3f317217, v8
	v_cmp_lt_f32_e64 vcc, |v8|, s64
	v_or_b32_e32 v4, 1, v2
	v_ashrrev_i32_e32 v5, 31, v4
	v_cndmask_b32_e32 v8, v8, v9, vcc
	v_cndmask_b32_e64 v9, 0, v103, s[4:5]
	v_sub_f32_e32 v8, v8, v9
	v_add_f32_e32 v9, v69, v8
	v_lshl_add_u32 v8, v14, 2, 0
	ds_write_b32 v8, v9
	v_lshl_add_u32 v8, v15, 2, 0
	s_waitcnt lgkmcnt(0)
	s_barrier
; #define LAS __attribute__((address_space(3)))
; __device__ __forceinline__ bf16 f2bf(float f) { return (bf16)(pk2(f, 0.f) & 0xffffu); }
; __device__ __forceinline__ void hgrn_x1_unit(const Args& a, int layer, int unit, LAS unsigned char* lds) {
;     ...
;     float off = 0.f, bl = 0.f;
; #pragma unroll
;     for (int g = 0; g < 4; ++g) { const float t = TOT[g * 128 + d]; bl += t; off += (g < tq) ? t : 0.f; }
;     unsigned kh[8];
; #pragma unroll
;     for (int i = 0; i < 8; ++i) {
;         const float bt = off + c[i];
;         const float qt = q[i] * __expf(bt), kh_ = kk[i] * __expf(bl - bt), kp = kk[i] * __expf(fminf(-bt, 80.f));
;         const int t = 8 * tq + i;
;         const bf16 qb = f2bf(qt);
;         *(LAS bf16*)(lds + HX_QL + t * 272 + d * 2) = qb;
;         *(LAS bf16*)(lds + HX_KP + t * 272 + d * 2) = f2bf(kp);
;         QT[(tok0 + t) * 1024 + h * 128 + d] = qb;
;         kh[i] = f2bf(kh_);
;     }
	ds_read2st64_b32 v[12:13], v8 offset1:2
	ds_read2st64_b32 v[28:29], v8 offset0:4 offset1:6
	v_sub_u32_e32 v8, v8, v82
	v_mad_u64_u32 v[38:39], s[6:7], v4, s74, v[8:9]
	v_lshl_add_u64 v[4:5], v[4:5], 0, s[46:47]
	v_lshlrev_b64 v[4:5], 11, v[4:5]
	v_lshl_add_u64 v[40:41], v[6:7], 0, v[4:5]
	v_or_b32_e32 v4, 2, v2
	v_ashrrev_i32_e32 v5, 31, v4
	v_lshl_add_u64 v[4:5], v[4:5], 0, s[46:47]
	v_lshlrev_b64 v[4:5], 11, v[4:5]
	v_lshl_add_u64 v[42:43], v[6:7], 0, v[4:5]
	v_or_b32_e32 v4, 3, v2
	v_ashrrev_i32_e32 v5, 31, v4
	v_lshl_add_u64 v[4:5], v[4:5], 0, s[46:47]
	v_lshlrev_b64 v[4:5], 11, v[4:5]
	v_lshl_add_u64 v[44:45], v[6:7], 0, v[4:5]
	v_or_b32_e32 v4, 4, v2
	v_ashrrev_i32_e32 v5, 31, v4
	v_lshl_add_u64 v[4:5], v[4:5], 0, s[46:47]
	v_lshlrev_b64 v[4:5], 11, v[4:5]
	v_lshlrev_b32_e32 v63, 16, v46
	v_lshl_add_u64 v[46:47], v[6:7], 0, v[4:5]
	v_or_b32_e32 v4, 5, v2
	v_ashrrev_i32_e32 v5, 31, v4
	v_lshl_add_u64 v[4:5], v[4:5], 0, s[46:47]
	v_lshlrev_b64 v[4:5], 11, v[4:5]
	v_cmp_lt_i32_e32 vcc, 1, v16
	v_lshl_add_u64 v[48:49], v[6:7], 0, v[4:5]
	v_or_b32_e32 v4, 6, v2
	v_mul_f32_e32 v23, v24, v23
	s_waitcnt lgkmcnt(1)
	v_cndmask_b32_e32 v24, 0, v13, vcc
	v_cmp_lt_i32_e32 vcc, 2, v16
	v_ashrrev_i32_e32 v5, 31, v4
	v_lshl_add_u64 v[4:5], v[4:5], 0, s[46:47]
	s_waitcnt lgkmcnt(0)
	v_cndmask_b32_e32 v31, 0, v28, vcc
	v_cmp_lt_i32_e32 vcc, 3, v16
	v_lshlrev_b64 v[50:51], 11, v[4:5]
	v_add_f32_e32 v4, 0, v12
	v_cndmask_b32_e32 v33, 0, v29, vcc
	v_cmp_lt_i32_e32 vcc, 0, v16
	v_mov_b32_e32 v30, v13
	v_mov_b32_e32 v32, v28
	v_cndmask_b32_e32 v5, 0, v4, vcc
	v_add_f32_e32 v5, v5, v24
	v_pk_add_f32 v[4:5], v[4:5], v[30:31]
	v_mad_u64_u32 v[34:35], s[6:7], v16, s73, v[8:9]
	v_pk_add_f32 v[12:13], v[4:5], v[32:33]
	v_mov_b32_e32 v8, v29
	v_add_f32_e32 v22, v22, v13
	v_mul_f32_e32 v4, 0x3fb8aa3b, v22
	v_exp_f32_e32 v24, v4
	v_pk_add_f32 v[4:5], v[12:13], v[8:9]
	s_lshl_b64 s[4:5], s[12:13], 13
	v_sub_f32_e32 v8, v4, v22
	v_mul_f32_e32 v8, 0x3fb8aa3b, v8
	v_exp_f32_e32 v12, v8
	v_min_f32_e64 v8, -v22, s76
	v_mul_f32_e32 v8, 0x3fb8aa3b, v8
	v_exp_f32_e32 v22, v8
	v_mul_f32_e32 v20, v24, v20
	v_mul_f32_e32 v12, v21, v12
	v_cvt_pk_bf16_f32 v20, v20, v83
	v_mul_f32_e32 v21, v21, v22
	ds_write_b16 v34, v20 offset:2048
	v_cvt_pk_bf16_f32 v21, v21, v83
	s_nop 0
	v_add_f32_e32 v20, v53, v13
	ds_write_b16 v34, v21 offset:10752
	v_mul_f32_e32 v21, 0x3fb8aa3b, v20
	v_sub_f32_e32 v22, v4, v20
	v_min_f32_e64 v20, -v20, s76
	v_exp_f32_e32 v21, v21
	v_mul_f32_e32 v20, 0x3fb8aa3b, v20
	v_exp_f32_e32 v20, v20
	v_mul_f32_e32 v22, 0x3fb8aa3b, v22
	v_exp_f32_e32 v22, v22
	v_mul_f32_e32 v19, v21, v19
	v_cvt_pk_bf16_f32 v12, v12, v83
	v_mul_f32_e32 v20, v52, v20
	v_cvt_pk_bf16_f32 v19, v19, v83
	ds_write_b16 v38, v19 offset:2048
	v_cvt_pk_bf16_f32 v20, v20, v83
	s_nop 0
	v_add_f32_e32 v19, v56, v13
	v_mul_f32_e32 v21, v52, v22
	ds_write_b16 v38, v20 offset:10752
	v_mul_f32_e32 v20, 0x3fb8aa3b, v19
	v_sub_f32_e32 v22, v4, v19
	v_min_f32_e64 v19, -v19, s76
	v_exp_f32_e32 v20, v20
	v_mul_f32_e32 v19, 0x3fb8aa3b, v19
	v_mul_f32_e32 v22, 0x3fb8aa3b, v22
	v_exp_f32_e32 v19, v19
	v_exp_f32_e32 v22, v22
	v_mul_f32_e32 v20, v20, v54
	v_cvt_pk_bf16_f32 v21, v21, v83
	v_mul_f32_e32 v19, v55, v19
	v_cvt_pk_bf16_f32 v20, v20, v83
	v_mul_f32_e32 v22, v55, v22
	ds_write_b16 v38, v20 offset:2320
	v_cvt_pk_bf16_f32 v19, v19, v83
	s_nop 0
	v_add_f32_e32 v20, v59, v13
	ds_write_b16 v38, v19 offset:11024
	v_cvt_pk_bf16_f32 v19, v22, v83
	v_mul_f32_e32 v22, 0x3fb8aa3b, v20
	v_sub_f32_e32 v24, v4, v20
	v_min_f32_e64 v20, -v20, s76
	v_mul_f32_e32 v20, 0x3fb8aa3b, v20
	v_exp_f32_e32 v22, v22
	v_exp_f32_e32 v20, v20
	v_mul_f32_e32 v24, 0x3fb8aa3b, v24
	v_exp_f32_e32 v24, v24
	v_mul_f32_e32 v22, v22, v57
	v_mul_f32_e32 v20, v58, v20
	v_cvt_pk_bf16_f32 v22, v22, v83
	ds_write_b16 v38, v22 offset:2592
	v_cvt_pk_bf16_f32 v20, v20, v83
	ds_write_b16 v38, v20 offset:11296
	v_add_f32_e32 v20, v62, v13
	s_nop 0
	v_mul_f32_e32 v22, 0x3fb8aa3b, v20
	v_sub_f32_e32 v28, v4, v20
	v_min_f32_e64 v20, -v20, s76
	v_exp_f32_e32 v22, v22
	v_mul_f32_e32 v20, 0x3fb8aa3b, v20
	v_mul_f32_e32 v28, 0x3fb8aa3b, v28
	v_exp_f32_e32 v20, v20
	v_exp_f32_e32 v28, v28
	v_mul_f32_e32 v24, v58, v24
	v_mul_f32_e32 v22, v22, v60
	v_cvt_pk_bf16_f32 v24, v24, v83
	v_mul_f32_e32 v20, v61, v20
	v_cvt_pk_bf16_f32 v22, v22, v83
	v_mul_f32_e32 v28, v61, v28
	ds_write_b16 v38, v22 offset:2864
	v_cvt_pk_bf16_f32 v20, v20, v83
	s_nop 0
	v_add_f32_e32 v22, v65, v13
	ds_write_b16 v38, v20 offset:11568
	v_cvt_pk_bf16_f32 v20, v28, v83
	v_mul_f32_e32 v28, 0x3fb8aa3b, v22
	v_sub_f32_e32 v29, v4, v22
	v_min_f32_e64 v22, -v22, s76
	v_mul_f32_e32 v22, 0x3fb8aa3b, v22
	v_exp_f32_e32 v28, v28
	v_exp_f32_e32 v22, v22
	v_add_f32_e32 v13, v69, v13
	v_mul_f32_e32 v29, 0x3fb8aa3b, v29
	v_mul_f32_e32 v28, v28, v63
	v_mul_f32_e32 v22, v64, v22
	v_cvt_pk_bf16_f32 v28, v28, v83
	ds_write_b16 v38, v28 offset:3136
	v_cvt_pk_bf16_f32 v22, v22, v83
	ds_write_b16 v38, v22 offset:11840
	s_nop 0
	v_mul_f32_e32 v22, 0x3fb8aa3b, v13
	v_sub_f32_e32 v28, v4, v13
	v_min_f32_e64 v13, -v13, s76
	v_mul_f32_e32 v13, 0x3fb8aa3b, v13
	v_exp_f32_e32 v29, v29
	v_exp_f32_e32 v22, v22
	v_exp_f32_e32 v13, v13
	v_lshl_add_u64 v[8:9], v[6:7], 0, v[50:51]
	v_mul_f32_e32 v29, v64, v29
	v_mul_f32_e32 v22, v22, v66
	v_mul_f32_e32 v13, v68, v13
	v_mul_f32_e32 v28, 0x3fb8aa3b, v28
	v_cvt_pk_bf16_f32 v29, v29, v83
	v_cvt_pk_bf16_f32 v22, v22, v83
	ds_write_b16 v38, v22 offset:3408
	v_cvt_pk_bf16_f32 v13, v13, v83
	v_exp_f32_e32 v28, v28
	ds_write_b16 v38, v13 offset:12112
	s_nop 0
	v_mul_f32_e32 v9, 0x3fb8aa3b, v5
	v_sub_f32_e32 v13, v4, v5
	v_min_f32_e64 v5, -v5, s76
	v_exp_f32_e32 v9, v9
	v_mul_f32_e32 v13, 0x3fb8aa3b, v13
	v_mul_f32_e32 v5, 0x3fb8aa3b, v5
	v_exp_f32_e32 v13, v13
	v_exp_f32_e32 v5, v5
	v_mul_f32_e32 v28, v68, v28
	v_cvt_pk_bf16_f32 v8, v28, v83
	v_mul_f32_e32 v9, v9, v70
	v_and_b32_e32 v22, 0xffff, v8
	v_or_b32_e32 v8, 7, v2
	v_mul_f32_e32 v13, v23, v13
	v_mul_f32_e32 v5, v23, v5
	v_cvt_pk_bf16_f32 v23, v9, v83
	v_ashrrev_i32_e32 v9, 31, v8
	v_lshl_add_u64 v[8:9], v[8:9], 0, s[46:47]
	s_add_u32 s4, s42, s4
	v_lshlrev_b64 v[8:9], 11, v[8:9]
	s_addc_u32 s5, s43, s5
	v_and_b32_e32 v19, 0xffff, v19
	v_lshl_add_u64 v[6:7], v[6:7], 0, v[8:9]
	v_lshlrev_b32_e32 v82, 6, v15
	ds_write_b16 v38, v23 offset:3680
	v_cvt_pk_bf16_f32 v5, v5, v83
	s_nop 0
	v_perm_b32 v8, v26, v11, s77
	v_perm_b32 v6, v17, v18, s77
	v_lshl_or_b32 v11, v24, 16, v19
	v_lshl_add_u64 v[18:19], s[4:5], 0, v[82:83]
	v_lshl_add_u64 v[2:3], v[2:3], 1, v[18:19]
	v_add_co_u32_e32 v18, vcc, s78, v2
	s_waitcnt vmcnt(0)
; #define LAS __attribute__((address_space(3)))
; __device__ __forceinline__ unsigned pk2(float lo, float hi) { unsigned r; asm volatile("v_cvt_pk_bf16_f32 %0, %1, %2" : "=v"(r) : "v"(lo), "v"(hi)); return r; }
; __device__ __forceinline__ f32x4 mfma16(bf16x8 a, bf16x8 b, f32x4 c) { return __builtin_amdgcn_mfma_f32_16x16x32_bf16(a, b, c, 0, 0, 0); }
; __device__ __forceinline__ void hgrn_x1_unit(const Args& a, int layer, int unit, LAS unsigned char* lds) {
;     ...
;     { u32x4 o; o.x = kh[0] | (kh[1] << 16); o.y = kh[2] | (kh[3] << 16); o.z = kh[4] | (kh[5] << 16); o.w = kh[6] | (kh[7] << 16); *(u32x4*)(KT + d * 32 + 8 * tq) = o;
;       u32x4 w; w.x = vv[0] | ((unsigned)vv[1] << 16); w.y = vv[2] | ((unsigned)vv[3] << 16); w.z = vv[4] | ((unsigned)vv[5] << 16); w.w = vv[6] | ((unsigned)vv[7] << 16);
;       *(u32x4*)(VT + d * 32 + 8 * tq) = w; *(LAS u32x4*)(lds + HX_VL + d * 80 + 16 * tq) = w; }
;     if (tq == 0) DEC[d] = __expf(bl);
;     __syncthreads();
;     const int fr = lane & 15, fg = lane >> 4, tt = wave & 1, vp = wave >> 1;
;     f32x4 sc[2];
; #pragma unroll
;     for (int st = 0; st < 2; ++st) { f32x4 acc = (f32x4){0.f, 0.f, 0.f, 0.f};
; #pragma unroll
;         for (int ks = 0; ks < 4; ++ks) {
;             const bf16x8 A = *(const LAS bf16x8*)(lds + HX_KP + (16 * st + fr) * 272 + (32 * ks + 8 * fg) * 2);
;             const bf16x8 B = *(const LAS bf16x8*)(lds + HX_QL + (16 * tt + fr) * 272 + (32 * ks + 8 * fg) * 2);
;             acc = mfma16(A, B, acc); }
; #pragma unroll
;         for (int r = 0; r < 4; ++r) acc[r] = (16 * st + 4 * fg + r <= 16 * tt + fr) ? acc[r] : 0.f;
;         sc[st] = acc; }
;     FragU P; P.u.x = pk2(sc[0][0], sc[0][1]); P.u.y = pk2(sc[0][2], sc[0][3]); P.u.z = pk2(sc[1][0], sc[1][1]); P.u.w = pk2(sc[1][2], sc[1][3]);
; #pragma unroll
;     for (int vi = 0; vi < 2; ++vi) { const int vt = 2 * vp + vi;
;         FragU V; V.h[0] = *(const LAS u32x2*)(lds + HX_VL + (16 * vt + fr) * 80 + (4 * fg) * 2); V.h[1] = *(const LAS u32x2*)(lds + HX_VL + (16 * vt + fr) * 80 + (16 + 4 * fg) * 2);
;         const f32x4 o = mfma16(P.v, V.v, (f32x4){0.f, 0.f, 0.f, 0.f});
; #pragma unroll
;         for (int r = 0; r < 4; ++r) OI[(tok0 + 16 * tt + 4 * fg + r) * 1024 + h * 128 + 16 * vt + fr] = o[r]; }
	v_perm_b32 v9, v27, v67, s77
	v_addc_co_u32_e32 v19, vcc, 0, v3, vcc
	v_add_co_u32_e32 v2, vcc, 0x47c82000, v2
	v_perm_b32 v7, v25, v10, s77
	s_nop 0
	v_addc_co_u32_e32 v3, vcc, 0, v3, vcc
	v_and_b32_e32 v12, 0xffff, v12
	v_and_b32_e32 v20, 0xffff, v20
	ds_write_b16 v38, v5 offset:12384
	v_cvt_pk_bf16_f32 v5, v13, v83
	global_store_dwordx4 v[2:3], v[6:9], off
	v_mul_u32_u24_e32 v2, 0x50, v15
	v_lshlrev_b32_e32 v3, 4, v16
	v_lshl_or_b32 v10, v21, 16, v12
	v_lshl_or_b32 v12, v29, 16, v20
	v_lshl_or_b32 v13, v5, 16, v22
	v_add3_u32 v2, 0, v2, v3
	v_cmp_gt_u32_e32 vcc, s80, v14
	global_store_dwordx4 v[18:19], v[10:13], off
	ds_write_b128 v2, v[6:9] offset:19456
	s_and_saveexec_b64 s[4:5], vcc
	s_cbranch_execz .LBB0_1393
	s_lshl_b64 s[6:7], s[12:13], 9
	s_add_u32 s6, s42, s6
	v_mul_f32_e32 v4, 0x3fb8aa3b, v4
	s_addc_u32 s7, s43, s7
	v_lshlrev_b32_e32 v82, 2, v15
	v_exp_f32_e32 v4, v4
	v_lshl_add_u64 v[2:3], s[6:7], 0, v[82:83]
	v_add_co_u32_e32 v2, vcc, 0x48c82000, v2
	s_nop 1
	v_addc_co_u32_e32 v3, vcc, 0, v3, vcc
	global_store_dword v[2:3], v4, off
.LBB0_1393:
	s_or_b64 exec, exec, s[4:5]
	v_and_b32_e32 v34, 15, v14
	v_bfe_u32 v35, v14, 4, 2
	v_lshlrev_b32_e32 v6, 4, v35
	v_mul_u32_u24_e32 v2, 0x110, v34
	v_add3_u32 v37, 0, v2, v6
	s_waitcnt lgkmcnt(0)
	s_barrier
	v_lshrrev_b32_e32 v241, 6, v0
	v_and_b32_e32 v242, 63, v0
	v_and_b32_e32 v240, 15, v242
	v_lshrrev_b32_e32 v243, 2, v241
	v_lshl_or_b32 v240, v243, 4, v240
	v_mul_u32_u24_e32 v240, 0x110, v240
	v_and_b32_e32 v243, 3, v241
	v_lshl_add_u32 v240, v243, 6, v240
	v_lshrrev_b32_e32 v243, 4, v242
	v_lshl_add_u32 v240, v243, 3, v240
	ds_read_b64 v[244:245], v240 offset:2048
	ds_read_b64 v[246:247], v240 offset:2080
	v_lshlrev_b32_e32 v248, 4, v0
	v_mov_b32_e32 v249, s12
	v_lshl_add_u32 v248, v249, 13, v248
	v_add_u32_e32 v248, 0x45c82000, v248
	v_mov_b32_e32 v249, 0
	v_lshl_add_u64 v[248:249], s[42:43], 0, v[248:249]
	s_waitcnt lgkmcnt(0)
	global_store_dwordx4 v[248:249], v[244:247], off
	ds_read_b128 v[2:5], v37 offset:10752
	s_lshr_b32 s4, s49, 2
	s_and_b32 s5, s4, 16
	v_or_b32_e32 v36, s5, v34
	v_mul_u32_u24_e32 v7, 0x110, v36
	v_add3_u32 v26, 0, v7, v6
	ds_read_b128 v[6:9], v37 offset:10816
	ds_read_b128 v[10:13], v26 offset:2048
	ds_read_b128 v[14:17], v26 offset:2112
	ds_read_b128 v[18:21], v37 offset:10880
	s_waitcnt lgkmcnt(2)
	v_mfma_f32_16x16x32_bf16 v[2:5], v[2:5], v[10:13], 0
	v_lshlrev_b32_e32 v38, 2, v35
	v_cmp_le_u32_e32 vcc, v38, v36
	s_ashr_i32 s4, s49, 2
	s_waitcnt lgkmcnt(1)
	v_mfma_f32_16x16x32_bf16 v[2:5], v[6:9], v[14:17], v[2:5]
	ds_read_b128 v[6:9], v37 offset:10944
	ds_read_b128 v[22:25], v26 offset:2176
	ds_read_b128 v[26:29], v26 offset:2240
	ds_read_b128 v[30:33], v37 offset:15168
	s_andn2_b32 s4, s4, 31
	s_waitcnt lgkmcnt(2)
	v_mfma_f32_16x16x32_bf16 v[2:5], v[18:21], v[22:25], v[2:5]
	ds_read_b128 v[18:21], v37 offset:15104
	v_lshlrev_b32_e32 v82, 2, v34
	s_waitcnt lgkmcnt(2)
	v_mfma_f32_16x16x32_bf16 v[2:5], v[6:9], v[26:29], v[2:5]
	ds_read_b128 v[6:9], v37 offset:15232
	s_waitcnt lgkmcnt(1)
	v_mfma_f32_16x16x32_bf16 v[10:13], v[18:21], v[10:13], 0
	ds_read_b128 v[18:21], v37 offset:15296
	s_nop 3
	v_cndmask_b32_e32 v39, 0, v2, vcc
	v_cmp_lt_u32_e32 vcc, v38, v36
	v_mfma_f32_16x16x32_bf16 v[10:13], v[30:33], v[14:17], v[10:13]
	v_or_b32_e32 v2, 2, v38
	v_cndmask_b32_e32 v40, 0, v3, vcc
	v_cmp_le_u32_e32 vcc, v2, v36
	s_waitcnt lgkmcnt(1)
	v_mfma_f32_16x16x32_bf16 v[6:9], v[6:9], v[22:25], v[10:13]
	v_or_b32_e32 v2, 3, v38
	v_cndmask_b32_e32 v14, 0, v4, vcc
	v_cmp_le_u32_e32 vcc, v2, v36
	v_or_b32_e32 v11, s4, v34
	v_or_b32_e32 v12, s5, v38
	v_cndmask_b32_e32 v10, 0, v5, vcc
	s_waitcnt lgkmcnt(0)
	v_mfma_f32_16x16x32_bf16 v[2:5], v[18:21], v[26:29], v[6:9]
	v_or_b32_e32 v18, s46, v12
	v_lshl_add_u64 v[12:13], s[42:43], 0, v[82:83]
	s_ashr_i32 s5, s4, 31
	v_or_b32_e32 v6, 16, v38
	v_cmp_le_u32_e32 vcc, v6, v36
	v_lshl_or_b32 v22, v18, 10, s48
	v_lshlrev_b32_e32 v82, 2, v22
	s_nop 0
	v_cndmask_b32_e32 v6, 0, v2, vcc
	v_or_b32_e32 v2, 17, v38
	v_cmp_le_u32_e32 vcc, v2, v36
	v_or_b32_e32 v2, 18, v38
	s_nop 0
	v_cndmask_b32_e32 v7, 0, v3, vcc
	v_cmp_le_u32_e32 vcc, v2, v36
	v_or_b32_e32 v2, 19, v38
	s_nop 0
	v_cndmask_b32_e32 v8, 0, v4, vcc
	v_cmp_le_u32_e32 vcc, v2, v36
	v_cvt_pk_bf16_f32 v2, v39, v40
	v_cvt_pk_bf16_f32 v3, v14, v10
	v_lshl_add_u32 v10, v35, 3, 0
	v_cvt_pk_bf16_f32 v4, v6, v7
	v_mad_u64_u32 v[6:7], s[6:7], v11, s79, v[10:11]
	v_cndmask_b32_e32 v5, 0, v5, vcc
	v_add_u32_e32 v6, 0x4800, v6
	v_cvt_pk_bf16_f32 v5, v8, v5
	ds_read2_b64 v[6:9], v6 offset0:128 offset1:132
	v_lshl_add_u64 v[14:15], s[4:5], 2, v[12:13]
	s_waitcnt lgkmcnt(0)
	v_mfma_f32_16x16x32_bf16 v[6:9], v[2:5], v[6:9], 0
	v_lshl_add_u64 v[16:17], v[14:15], 0, s[22:23]
	v_lshl_add_u64 v[18:19], v[16:17], 0, v[82:83]
	v_or_b32_e32 v82, 0x400, v22
	v_lshlrev_b64 v[20:21], 2, v[82:83]
	v_lshl_add_u64 v[12:13], v[16:17], 0, v[20:21]
	v_or_b32_e32 v82, 0x800, v22
	s_nop 1
	v_lshrrev_b32_e32 v250, 6, v0
	v_and_b32_e32 v251, 1, v250
	v_lshrrev_b32_e32 v250, 1, v250
	v_lshlrev_b32_e32 v250, 11, v250
	v_lshl_or_b32 v250, v251, 13, v250
	v_and_b32_e32 v251, 63, v0
	v_lshl_or_b32 v250, v251, 4, v250
	v_mov_b32_e32 v251, s12
	v_lshl_add_u32 v250, v251, 14, v250
	v_add_u32_e32 v250, 0x4b182000, v250
	v_mov_b32_e32 v251, 0
	v_lshl_add_u64 v[250:251], s[42:43], 0, v[250:251]
	global_store_dwordx4 v[250:251], v[6:9], off
	s_nop 1
	v_lshlrev_b64 v[6:7], 2, v[82:83]
	v_lshl_add_u64 v[12:13], v[16:17], 0, v[6:7]
	s_nop 0
	v_or_b32_e32 v8, 16, v11
	v_mad_u64_u32 v[10:11], s[4:5], v8, s79, v[10:11]
	v_add_u32_e32 v8, 0x4800, v10
	ds_read2_b64 v[10:13], v8 offset0:128 offset1:132
	v_or_b32_e32 v82, 0xc00, v22
	v_lshlrev_b64 v[22:23], 2, v[82:83]
	s_waitcnt lgkmcnt(0)
	v_mfma_f32_16x16x32_bf16 v[2:5], v[2:5], v[10:13], 0
	v_lshl_add_u64 v[16:17], v[16:17], 0, v[22:23]
	s_nop 0
	v_lshl_add_u64 v[8:9], v[14:15], 0, s[24:25]
	v_lshl_add_u64 v[10:11], v[8:9], 0, v[20:21]
	s_nop 3
	global_store_dwordx4 v[250:251], v[2:5], off offset:1024
	s_nop 1
	v_lshl_add_u64 v[2:3], v[8:9], 0, v[6:7]
	s_nop 0
	v_lshl_add_u64 v[2:3], v[8:9], 0, v[22:23]
	s_nop 0
	s_mov_b64 s[4:5], 0

; __device__ __forceinline__ void hgrn_x2_unit(const Args& a, int unit) {
;     int tid = threadIdx.x; asm volatile("" : "+v"(tid)); const int lane = tid & 63;
;     size_t wz_ = 0; asm volatile("" : "+s"(wz_)); unsigned char* ws = a.ws + wz_;
;     const int vs = unit & 7, h = (unit >> 3) & 7, b = unit >> 6;
;     const bf16* QT = (const bf16*)(ws + WS_HQT); float* OI = (float*)(ws + WS_HOI);
;     const int fr = lane & 15, fg = lane >> 4;
;     f32x4 S[8];
; #pragma unroll
;     for (int i = 0; i < 8; ++i) S[i] = (f32x4){0.f, 0.f, 0.f, 0.f};
; #pragma unroll 1
;     for (int blk = 0; blk < SEQ / HB; ++blk) {
;         const int u = (b * 8 + h) * 64 + blk; const size_t tok0 = (size_t)b * SEQ + blk * HB;
;         const bf16* KT = (const bf16*)(ws + WS_HKT) + (size_t)u * 4096; const bf16* VT = (const bf16*)(ws + WS_HVT) + (size_t)u * 4096; const float* DEC = (const float*)(ws + WS_HDEC) + (size_t)u * 128;
;         FragU Aq[2][4]; f32x4 o[2]; FragU Ak[8]; f32x4 dc[8]; FragU Bv;
; #pragma unroll
;         for (int mt = 0; mt < 2; ++mt) { const bf16* qr = QT + (tok0 + 16 * mt + fr) * 1024 + h * 128;
; #pragma unroll
;             for (int ks = 0; ks < 4; ++ks) { Aq[mt][ks].h[0] = *(const u32x2*)(qr + 32 * ks + 4 * fg); Aq[mt][ks].h[1] = *(const u32x2*)(qr + 32 * ks + 16 + 4 * fg); }
; #pragma unroll
;             for (int r = 0; r < 4; ++r) o[mt][r] = OI[(tok0 + 16 * mt + 4 * fg + r) * 1024 + h * 128 + 16 * vs + fr]; }
; #pragma unroll
;         for (int dt = 0; dt < 8; ++dt) { Ak[dt].u = *(const u32x4*)(KT + (16 * dt + fr) * 32 + 8 * fg); dc[dt] = *(const f32x4*)(DEC + 16 * dt + 4 * fg); }
;         Bv.u = *(const u32x4*)(VT + (16 * vs + fr) * 32 + 8 * fg);
.LBB0_1793:
	v_mov_b32_e32 v1, v0
	s_mov_b64 s[4:5], -1
	v_readfirstlane_b32 s2, v1
	s_ashr_i32 s2, s2, 6
	s_and_b64 vcc, exec, s[14:15]
	s_cbranch_vccz .LBB0_1798
	s_cmpk_lt_i32 s60, 0x80
	s_cselect_b64 s[4:5], -1, 0
	s_cmp_lt_i32 s2, 2
	s_cselect_b64 s[6:7], -1, 0
	s_and_b64 s[4:5], s[4:5], s[6:7]
	s_andn2_b64 vcc, exec, s[4:5]
	s_cbranch_vccnz .LBB0_1797
	s_lshl_b32 s4, s60, 1
	s_add_i32 s14, s2, s4
	v_mov_b32_e32 v1, v0
	s_mov_b64 s[4:5], 0
	s_ashr_i32 s8, s14, 6
	s_load_dwordx2 s[6:7], s[0:1], 0xd0
	s_ashr_i32 s9, s8, 31
	s_waitcnt vmcnt(0)
	v_and_b32_e32 v4, 15, v1
	v_bfe_u32 v1, v1, 4, 2
	s_lshl_b64 s[10:11], s[8:9], 23
	s_bfe_u32 s15, s14, 0x30003
	v_lshl_or_b32 v2, v1, 14, s10
	s_and_b32 s14, s14, 7
	v_lshl_or_b32 v2, s15, 9, v2
	s_lshl_b32 s10, s14, 6
	v_lshlrev_b32_e32 v3, 2, v4
	s_lshl_b32 s16, s8, 9
	v_or3_b32 v2, v2, s10, v3
	v_mov_b32_e32 v3, s11
	s_lshl_b64 s[8:9], s[8:9], 22
	s_lshl_b32 s17, s15, 6
	v_lshlrev_b32_e32 v5, 3, v1
	s_waitcnt lgkmcnt(0)
	v_lshl_add_u64 v[46:47], s[6:7], 0, v[2:3]
	v_lshl_or_b32 v2, v4, 11, s8
	s_lshl_b32 s8, s15, 8
	v_or3_b32 v2, v2, s8, v5
	s_or_b32 s8, s16, s17
	v_mov_b32_e32 v3, s9
	s_ashr_i32 s9, s8, 31
	v_and_b32_e32 v250, 63, v0
	v_lshlrev_b32_e32 v250, 4, v250
	s_mul_i32 vcc_lo, s8, 0x2000
	v_add_u32_e32 v250, vcc_lo, v250
	v_mov_b32_e32 v251, 0
	v_lshl_add_u64 v[48:49], s[6:7], 0, v[250:251]
	v_and_b32_e32 v170, 63, v0
	v_lshlrev_b32_e32 v170, 4, v170
	s_mul_i32 vcc_lo, s8, 0x4000
	v_add_u32_e32 v170, vcc_lo, v170
	s_mul_i32 vcc_lo, s14, 0x400
	v_add_u32_e32 v170, vcc_lo, v170
	v_add_u32_e32 v170, 0x4b182000, v170
	v_add_u32_e32 v172, 0x2000, v170
	v_mov_b32_e32 v171, 0
	v_mov_b32_e32 v173, 0
	v_lshl_add_u64 v[170:171], s[6:7], 0, v[170:171]
	v_lshl_add_u64 v[172:173], s[6:7], 0, v[172:173]
	s_lshl_b64 s[10:11], s[8:9], 13
	v_lshlrev_b32_e32 v2, 4, v1
	v_or_b32_e32 v1, s10, v2
	s_lshl_b32 s10, s14, 10
	v_lshlrev_b32_e32 v8, 6, v4
	v_or3_b32 v4, s10, v8, v1
	v_mov_b32_e32 v5, s11
	v_lshl_add_u64 v[6:7], s[6:7], 0, v[4:5]
	v_or_b32_e32 v4, v1, v8
	s_lshl_b64 s[8:9], s[8:9], 9
	v_lshl_add_u64 v[52:53], s[6:7], 0, v[4:5]
	s_add_u32 s6, s6, s8
	v_mov_b32_e32 v3, 0
	s_addc_u32 s7, s7, s9
	s_mov_b64 s[10:11], 0x47c82000
	v_lshl_add_u64 v[4:5], s[6:7], 0, v[2:3]
	s_mov_b64 s[6:7], 0x48c82100
	v_lshl_add_u64 v[50:51], v[6:7], 0, s[10:11]
	v_lshl_add_u64 v[54:55], v[4:5], 0, s[6:7]
	s_mov_b32 s16, 64
	s_mov_b32 s17, 0x45c82000
	s_mov_b32 s18, 0x48d83000
	s_mov_b32 s19, 0x48d85000
	s_mov_b32 s20, 0x45c83000
	s_mov_b32 s21, 0x48d93000
	s_mov_b32 s22, 0x48d95000
	s_mov_b32 s23, 0x46c82000
	s_mov_b32 s24, 0x46c83000
	s_mov_b64 s[6:7], 0x20000
	s_mov_b64 s[8:9], 0x2000
	s_mov_b64 s[10:11], 0x2000
	s_mov_b64 s[14:15], 0x200
	v_mov_b32_e32 v2, v3
	v_mov_b32_e32 v4, v3
	v_mov_b32_e32 v5, v3
	v_mov_b32_e32 v6, v3
	v_mov_b32_e32 v7, v3
	v_mov_b32_e32 v8, v3
	v_mov_b32_e32 v9, v3
	v_mov_b32_e32 v10, v3
	v_mov_b32_e32 v11, v3
	v_mov_b32_e32 v12, v3
	v_mov_b32_e32 v13, v3
	v_mov_b32_e32 v14, v3
	v_mov_b32_e32 v15, v3
	v_mov_b32_e32 v16, v3
	v_mov_b32_e32 v17, v3
	v_mov_b32_e32 v18, v3
	v_mov_b32_e32 v19, v3
	v_mov_b32_e32 v20, v3
	v_mov_b32_e32 v21, v3
	v_mov_b32_e32 v22, v3
	v_mov_b32_e32 v23, v3
	v_mov_b32_e32 v24, v3
	v_mov_b32_e32 v25, v3
	v_mov_b32_e32 v26, v3
	v_mov_b32_e32 v27, v3
	v_mov_b32_e32 v28, v3
	v_mov_b32_e32 v29, v3
	v_mov_b32_e32 v30, v3
	v_mov_b32_e32 v31, v3
	v_mov_b32_e32 v32, v3
	v_mov_b32_e32 v33, v3
; __device__ __forceinline__ unsigned pk2(float lo, float hi) { unsigned r; asm volatile("v_cvt_pk_bf16_f32 %0, %1, %2" : "=v"(r) : "v"(lo), "v"(hi)); return r; }
; __device__ __forceinline__ f32x4 mfma16(bf16x8 a, bf16x8 b, f32x4 c) { return __builtin_amdgcn_mfma_f32_16x16x32_bf16(a, b, c, 0, 0, 0); }
; __device__ __forceinline__ void hgrn_x2_unit(const Args& a, int unit) {
;     ...
;     for (int blk = 0; blk < SEQ / HB; ++blk) {
;         const int u = (b * 8 + h) * 64 + blk; const size_t tok0 = (size_t)b * SEQ + blk * HB;
;         const bf16* KT = (const bf16*)(ws + WS_HKT) + (size_t)u * 4096; const bf16* VT = (const bf16*)(ws + WS_HVT) + (size_t)u * 4096; const float* DEC = (const float*)(ws + WS_HDEC) + (size_t)u * 128;
;         FragU Aq[2][4]; f32x4 o[2]; FragU Ak[8]; f32x4 dc[8]; FragU Bv;
; #pragma unroll
;         for (int mt = 0; mt < 2; ++mt) { const bf16* qr = QT + (tok0 + 16 * mt + fr) * 1024 + h * 128;
; #pragma unroll
;             for (int ks = 0; ks < 4; ++ks) { Aq[mt][ks].h[0] = *(const u32x2*)(qr + 32 * ks + 4 * fg); Aq[mt][ks].h[1] = *(const u32x2*)(qr + 32 * ks + 16 + 4 * fg); }
; #pragma unroll
;             for (int r = 0; r < 4; ++r) o[mt][r] = OI[(tok0 + 16 * mt + 4 * fg + r) * 1024 + h * 128 + 16 * vs + fr]; }
; #pragma unroll
;         for (int dt = 0; dt < 8; ++dt) { Ak[dt].u = *(const u32x4*)(KT + (16 * dt + fr) * 32 + 8 * fg); dc[dt] = *(const f32x4*)(DEC + 16 * dt + 4 * fg); }
;         Bv.u = *(const u32x4*)(VT + (16 * vs + fr) * 32 + 8 * fg);
; #pragma unroll
;         for (int ks = 0; ks < 4; ++ks) { FragU Sb; Sb.u.x = pk2(S[2 * ks][0], S[2 * ks][1]); Sb.u.y = pk2(S[2 * ks][2], S[2 * ks][3]); Sb.u.z = pk2(S[2 * ks + 1][0], S[2 * ks + 1][1]); Sb.u.w = pk2(S[2 * ks + 1][2], S[2 * ks + 1][3]);
;             o[0] = mfma16(Aq[0][ks].v, Sb.v, o[0]); o[1] = mfma16(Aq[1][ks].v, Sb.v, o[1]); }
; #pragma unroll
;         for (int mt = 0; mt < 2; ++mt)
; #pragma unroll
;             for (int r = 0; r < 4; ++r) OI[(tok0 + 16 * mt + 4 * fg + r) * 1024 + h * 128 + 16 * vs + fr] = o[mt][r];
; #pragma unroll
;         for (int dt = 0; dt < 8; ++dt) S[dt] = mfma16(Ak[dt].v, Bv.v, S[dt] * dc[dt]);
;     }
.LBB0_1796:
	v_lshl_add_u64 v[34:35], v[48:49], 0, s[4:5]
	v_add_co_u32_e32 v120, vcc, s17, v34
	v_lshl_add_u64 v[36:37], v[46:47], 0, s[4:5]
	s_nop 0
	v_addc_co_u32_e32 v121, vcc, 0, v35, vcc
	v_add_co_u32_e32 v56, vcc, s18, v36
	v_lshl_add_u64 v[40:41], v[52:53], 0, s[4:5]
	s_nop 0
	v_addc_co_u32_e32 v57, vcc, 0, v37, vcc
	v_add_co_u32_e32 v58, vcc, s19, v36
	v_lshl_add_u64 v[38:39], v[54:55], 0, s[4:5]
	s_nop 0
	v_addc_co_u32_e32 v59, vcc, 0, v37, vcc
	v_add_co_u32_e32 v122, vcc, s20, v34
	v_lshl_add_u64 v[156:157], v[50:51], 0, s[4:5]
	s_nop 0
	v_addc_co_u32_e32 v123, vcc, 0, v35, vcc
	v_add_co_u32_e32 v60, vcc, s21, v36
	s_add_i32 s16, s16, -1
	s_nop 0
	v_addc_co_u32_e32 v61, vcc, 0, v37, vcc
	v_add_co_u32_e32 v62, vcc, s22, v36
	v_lshl_add_u64 v[46:47], v[46:47], 0, s[6:7]
	s_nop 0
	v_addc_co_u32_e32 v63, vcc, 0, v37, vcc
	v_add_co_u32_e32 v132, vcc, s23, v40
	v_lshl_add_u64 v[48:49], v[48:49], 0, s[8:9]
	s_nop 0
	v_addc_co_u32_e32 v133, vcc, 0, v41, vcc
	v_add_co_u32_e32 v152, vcc, s24, v40
	v_lshl_add_u64 v[50:51], v[50:51], 0, s[10:11]
	s_nop 0
	v_addc_co_u32_e32 v153, vcc, 0, v41, vcc
	global_load_dwordx4 v[64:67], v[38:39], off offset:-256
	global_load_dwordx4 v[68:71], v[38:39], off offset:-192
	global_load_dwordx4 v[72:75], v[38:39], off offset:-128
	global_load_dwordx4 v[76:79], v[38:39], off offset:-64
	global_load_dwordx4 v[80:83], v[38:39], off
	global_load_dwordx4 v[84:87], v[38:39], off offset:64
	global_load_dwordx4 v[88:91], v[38:39], off offset:128
	global_load_dwordx4 v[92:95], v[38:39], off offset:192
	global_load_dwordx4 v[96:99], v[120:121], off
	s_nop 0
	global_load_dwordx4 v[100:103], v[120:121], off offset:1024
	s_nop 0
	global_load_dwordx4 v[104:107], v[120:121], off offset:2048
	s_nop 0
	global_load_dwordx4 v[34:37], v[120:121], off offset:3072
	s_nop 0
	global_load_dwordx4 v[108:111], v[122:123], off
	s_nop 0
	global_load_dwordx4 v[112:115], v[122:123], off offset:1024
	s_nop 0
	global_load_dwordx4 v[42:45], v[122:123], off offset:2048
	s_nop 0
	global_load_dwordx4 v[38:41], v[122:123], off offset:3072
	s_nop 0
	global_load_dwordx4 v[116:119], v[170:171], off
	s_nop 0
	s_nop 0
	s_nop 0
	global_load_dwordx4 v[120:123], v[172:173], off
	s_nop 0
	s_nop 0
	s_nop 0
	global_load_dwordx4 v[124:127], v[132:133], off offset:1024
	global_load_dwordx4 v[128:131], v[132:133], off offset:2048
	s_nop 0
	global_load_dwordx4 v[132:135], v[132:133], off offset:3072
	s_nop 0
	global_load_dwordx4 v[136:139], v[152:153], off offset:-4096
	global_load_dwordx4 v[140:143], v[152:153], off
	global_load_dwordx4 v[144:147], v[152:153], off offset:1024
	global_load_dwordx4 v[148:151], v[152:153], off offset:2048
	s_nop 0
	global_load_dwordx4 v[152:155], v[152:153], off offset:3072
	s_nop 0
	global_load_dwordx4 v[156:159], v[156:157], off
	v_lshl_add_u64 v[170:171], v[170:171], 0, s[10:11]
	v_lshl_add_u64 v[170:171], v[170:171], 0, s[10:11]
	v_lshl_add_u64 v[172:173], v[172:173], 0, s[10:11]
	v_lshl_add_u64 v[172:173], v[172:173], 0, s[10:11]
	v_cvt_pk_bf16_f32 v160, v2, v3
	v_cvt_pk_bf16_f32 v161, v4, v5
	v_cvt_pk_bf16_f32 v162, v6, v7
	v_cvt_pk_bf16_f32 v163, v8, v9
	v_cvt_pk_bf16_f32 v164, v10, v11
	v_cvt_pk_bf16_f32 v165, v12, v13
	v_cvt_pk_bf16_f32 v166, v14, v15
	v_cvt_pk_bf16_f32 v167, v16, v17
	v_lshl_add_u64 v[52:53], v[52:53], 0, s[10:11]
	v_lshl_add_u64 v[54:55], v[54:55], 0, s[14:15]
	s_cmp_lg_u32 s16, 0
	s_waitcnt vmcnt(10)
	v_mfma_f32_16x16x32_bf16 v[96:99], v[96:99], v[160:163], v[116:119]
	v_mul_f32_e64 v6, v6, v68
	v_mul_f32_e64 v7, v7, v69
	v_pk_mul_f32 v[8:9], v[8:9], v[70:71]
	v_cvt_pk_bf16_f32 v116, v18, v19
	s_waitcnt vmcnt(9)
	v_mfma_f32_16x16x32_bf16 v[108:111], v[108:111], v[160:163], v[120:123]
	v_cvt_pk_bf16_f32 v117, v20, v21
	v_cvt_pk_bf16_f32 v118, v22, v23
	v_mul_f32_e64 v10, v10, v72
	v_mul_f32_e64 v11, v11, v73
	v_mfma_f32_16x16x32_bf16 v[68:71], v[100:103], v[164:167], v[96:99]
	v_mul_f32_e64 v12, v12, v74
	v_mul_f32_e64 v13, v13, v75
	v_cvt_pk_bf16_f32 v119, v24, v25
	v_pk_mul_f32 v[2:3], v[2:3], v[64:65]
	v_mfma_f32_16x16x32_bf16 v[72:75], v[112:115], v[164:167], v[108:111]
	v_mul_f32_e64 v4, v4, v66
	v_mul_f32_e64 v5, v5, v67
	v_pk_mul_f32 v[14:15], v[14:15], v[76:77]
	v_pk_mul_f32 v[16:17], v[16:17], v[78:79]
	v_mfma_f32_16x16x32_bf16 v[68:71], v[104:107], v[116:119], v[68:71]
	v_cvt_pk_bf16_f32 v64, v26, v27
	v_mul_f32_e64 v18, v18, v80
	v_mul_f32_e64 v19, v19, v81
	v_pk_mul_f32 v[20:21], v[20:21], v[82:83]
	v_cvt_pk_bf16_f32 v65, v28, v29
	v_pk_mul_f32 v[22:23], v[22:23], v[84:85]
	v_pk_mul_f32 v[24:25], v[24:25], v[86:87]
	v_cvt_pk_bf16_f32 v66, v30, v31
	v_pk_mul_f32 v[26:27], v[26:27], v[88:89]
	v_pk_mul_f32 v[28:29], v[28:29], v[90:91]
	v_cvt_pk_bf16_f32 v67, v32, v33
	v_pk_mul_f32 v[30:31], v[30:31], v[92:93]
	v_pk_mul_f32 v[32:33], v[32:33], v[94:95]
	s_waitcnt vmcnt(0)
	v_mfma_f32_16x16x32_bf16 v[2:5], v[136:139], v[156:159], v[2:5]
	v_mfma_f32_16x16x32_bf16 v[6:9], v[124:127], v[156:159], v[6:9]
	v_mfma_f32_16x16x32_bf16 v[10:13], v[128:131], v[156:159], v[10:13]
	v_mfma_f32_16x16x32_bf16 v[14:17], v[132:135], v[156:159], v[14:17]
	v_mfma_f32_16x16x32_bf16 v[18:21], v[140:143], v[156:159], v[18:21]
	v_mfma_f32_16x16x32_bf16 v[22:25], v[144:147], v[156:159], v[22:25]
	v_mfma_f32_16x16x32_bf16 v[26:29], v[148:151], v[156:159], v[26:29]
	v_mfma_f32_16x16x32_bf16 v[30:33], v[152:155], v[156:159], v[30:33]
	v_mfma_f32_16x16x32_bf16 v[42:45], v[42:45], v[116:119], v[72:75]
	v_mfma_f32_16x16x32_bf16 v[34:37], v[34:37], v[64:67], v[68:71]
	v_mfma_f32_16x16x32_bf16 v[38:41], v[38:41], v[64:67], v[42:45]
	s_nop 6
	global_store_dword v[56:57], v34, off offset:-4096
	global_store_dword v[56:57], v35, off
	global_store_dword v[58:59], v36, off offset:-4096
	global_store_dword v[58:59], v37, off
	global_store_dword v[60:61], v38, off offset:-4096
	global_store_dword v[60:61], v39, off
	global_store_dword v[62:63], v40, off offset:-4096
	global_store_dword v[62:63], v41, off
	s_cbranch_scc1 .LBB0_1796
